# GEMM K-loop heads (9 loops) aligned to 64-byte instruction-cache lines with s_nop padding
# speedup vs baseline: 1.0043x; 1.0043x over previous
.LBB0_161:
	s_ashr_i32 s29, s28, 31
	s_lshl_b64 s[30:31], s[28:29], 20
	v_readlane_b32 s34, v254, 18
	v_readlane_b32 s35, v254, 19
	s_add_u32 s30, s34, s30
	s_addc_u32 s31, s35, s31
	s_and_b64 s[34:35], s[12:13], exec
	s_cselect_b32 s15, s31, s17
	s_cselect_b32 s29, s30, s16
	s_ashr_i32 s27, s26, 31
	s_lshl_b64 s[34:35], s[26:27], 20
	s_add_u32 s34, s33, s34
	s_addc_u32 s35, s42, s35
	s_and_b64 s[38:39], s[12:13], exec
	s_cselect_b32 s27, s35, s37
	s_cselect_b32 s40, s34, s36
	s_add_u32 s16, s16, 0x80080
	s_addc_u32 s17, s17, 0
	s_add_u32 s41, s36, 0x100
	s_addc_u32 s64, s37, 0
	s_mov_b32 s65, -2
	ds_read_b128 v[90:93], v197
	ds_read_b128 v[94:97], v197 offset:1024
	ds_read_b128 v[98:101], v197 offset:2048
	ds_read_b128 v[102:105], v197 offset:3072
	ds_read_b128 v[146:149], v198
	ds_read_b128 v[150:153], v198 offset:1024
	ds_read_b128 v[180:183], v198 offset:2048
	ds_read_b128 v[184:187], v198 offset:3072
	s_add_u32 s36, s16, 0xfff80080
	s_addc_u32 s37, s17, -1
	s_cmp_eq_u32 s65, 28
	s_cselect_b32 s39, s15, s37
	s_cselect_b32 s38, s29, s36
	s_cselect_b32 s37, s27, s64
	s_cselect_b32 s36, s40, s41
	v_lshl_add_u64 v[212:213], s[16:17], 0, v[172:173]
	s_add_i32 m0, s44, 0xc000
	ds_read_b128 v[188:191], v199
	ds_read_b128 v[192:195], v199 offset:1024
	ds_read_b128 v[200:203], v199 offset:2048
	ds_read_b128 v[204:207], v199 offset:3072
	ds_read_b128 v[208:211], v199 offset:4096
	ds_read_b128 v[216:219], v199 offset:5120
	ds_read_b128 v[220:223], v199 offset:6144
	ds_read_b128 v[224:227], v199 offset:7168
	global_load_lds_dwordx4 v[212:213], off
	v_lshl_add_u64 v[212:213], s[16:17], 0, v[174:175]
	s_add_i32 m0, s44, 0xe000
	s_nop 0
	global_load_lds_dwordx4 v[212:213], off
	s_waitcnt vmcnt(8)
	s_waitcnt lgkmcnt(0)
	s_setprio 1
	s_barrier
	v_mfma_f32_16x16x32_bf16 v[70:73], v[90:93], v[188:191], 0
	v_mfma_f32_16x16x32_bf16 v[66:69], v[98:101], v[188:191], 0
	v_mfma_f32_16x16x32_bf16 v[54:57], v[90:93], v[200:203], 0
	v_mfma_f32_16x16x32_bf16 v[50:53], v[98:101], v[200:203], 0
	v_mfma_f32_16x16x32_bf16 v[46:49], v[90:93], v[208:211], 0
	v_mfma_f32_16x16x32_bf16 v[42:45], v[98:101], v[208:211], 0
	v_mfma_f32_16x16x32_bf16 v[38:41], v[90:93], v[220:223], 0
	v_mfma_f32_16x16x32_bf16 v[34:37], v[98:101], v[220:223], 0
	v_mfma_f32_16x16x32_bf16 v[70:73], v[94:97], v[192:195], v[70:73]
	v_mfma_f32_16x16x32_bf16 v[66:69], v[102:105], v[192:195], v[66:69]
	v_mfma_f32_16x16x32_bf16 v[54:57], v[94:97], v[204:207], v[54:57]
	v_mfma_f32_16x16x32_bf16 v[50:53], v[102:105], v[204:207], v[50:53]
	v_mfma_f32_16x16x32_bf16 v[46:49], v[94:97], v[216:219], v[46:49]
	v_mfma_f32_16x16x32_bf16 v[42:45], v[102:105], v[216:219], v[42:45]
	v_mfma_f32_16x16x32_bf16 v[38:41], v[94:97], v[224:227], v[38:41]
	v_mfma_f32_16x16x32_bf16 v[34:37], v[102:105], v[224:227], v[34:37]
	s_setprio 0
	s_setprio 1
	v_mfma_f32_16x16x32_bf16 v[142:145], v[146:149], v[188:191], 0
	v_mfma_f32_16x16x32_bf16 v[138:141], v[180:183], v[188:191], 0
	v_mfma_f32_16x16x32_bf16 v[134:137], v[146:149], v[200:203], 0
	v_mfma_f32_16x16x32_bf16 v[130:133], v[180:183], v[200:203], 0
	v_mfma_f32_16x16x32_bf16 v[126:129], v[146:149], v[208:211], 0
	v_mfma_f32_16x16x32_bf16 v[122:125], v[180:183], v[208:211], 0
	v_mfma_f32_16x16x32_bf16 v[118:121], v[146:149], v[220:223], 0
	v_mfma_f32_16x16x32_bf16 v[114:117], v[180:183], v[220:223], 0
	v_mfma_f32_16x16x32_bf16 v[142:145], v[150:153], v[192:195], v[142:145]
	v_mfma_f32_16x16x32_bf16 v[138:141], v[184:187], v[192:195], v[138:141]
	v_mfma_f32_16x16x32_bf16 v[134:137], v[150:153], v[204:207], v[134:137]
	v_mfma_f32_16x16x32_bf16 v[130:133], v[184:187], v[204:207], v[130:133]
	v_mfma_f32_16x16x32_bf16 v[126:129], v[150:153], v[216:219], v[126:129]
	v_mfma_f32_16x16x32_bf16 v[122:125], v[184:187], v[216:219], v[122:125]
	v_mfma_f32_16x16x32_bf16 v[118:121], v[150:153], v[224:227], v[118:121]
	v_mfma_f32_16x16x32_bf16 v[114:117], v[184:187], v[224:227], v[114:117]
	s_barrier
	s_setprio 0
	s_add_i32 s66, s57, s43
	v_lshl_add_u64 v[212:213], s[36:37], 0, v[156:157]
	s_mov_b32 m0, s66
	ds_read_b128 v[188:191], v199 offset:16384
	ds_read_b128 v[192:195], v199 offset:17408
	ds_read_b128 v[200:203], v199 offset:18432
	ds_read_b128 v[204:207], v199 offset:19456
	ds_read_b128 v[208:211], v199 offset:20480
	ds_read_b128 v[216:219], v199 offset:21504
	ds_read_b128 v[220:223], v199 offset:22528
	ds_read_b128 v[224:227], v199 offset:23552
	global_load_lds_dwordx4 v[212:213], off
	s_add_i32 m0, s66, 0x2000
	s_add_u32 s66, s36, 0x80000
	v_lshl_add_u64 v[214:215], s[36:37], 0, v[160:161]
	s_addc_u32 s67, s37, 0
	s_add_i32 s68, s58, s43
	global_load_lds_dwordx4 v[214:215], off
	v_lshl_add_u64 v[228:229], s[66:67], 0, v[156:157]
	s_mov_b32 m0, s68
	v_lshl_add_u64 v[230:231], s[38:39], 0, v[158:159]
	global_load_lds_dwordx4 v[228:229], off
	v_lshl_add_u64 v[228:229], s[66:67], 0, v[160:161]
	s_add_i32 m0, s68, 0x2000
	s_nop 0
	global_load_lds_dwordx4 v[228:229], off
	v_lshl_add_u64 v[228:229], s[38:39], 0, v[154:155]
	s_mov_b32 m0, s44
	s_nop 0
	global_load_lds_dwordx4 v[228:229], off
	s_mov_b32 m0, s45
	s_nop 0
	global_load_lds_dwordx4 v[230:231], off
	s_waitcnt vmcnt(8)
	s_waitcnt lgkmcnt(0)
	s_setprio 1
	s_barrier
	v_mfma_f32_16x16x32_bf16 v[30:33], v[90:93], v[188:191], 0
	v_mfma_f32_16x16x32_bf16 v[26:29], v[98:101], v[188:191], 0
	v_mfma_f32_16x16x32_bf16 v[22:25], v[90:93], v[200:203], 0
	v_mfma_f32_16x16x32_bf16 v[18:21], v[98:101], v[200:203], 0
	v_mfma_f32_16x16x32_bf16 v[14:17], v[90:93], v[208:211], 0
	v_mfma_f32_16x16x32_bf16 v[10:13], v[98:101], v[208:211], 0
	v_mfma_f32_16x16x32_bf16 v[6:9], v[90:93], v[220:223], 0
	v_mfma_f32_16x16x32_bf16 v[2:5], v[98:101], v[220:223], 0
	v_mfma_f32_16x16x32_bf16 v[30:33], v[94:97], v[192:195], v[30:33]
	v_mfma_f32_16x16x32_bf16 v[26:29], v[102:105], v[192:195], v[26:29]
	v_mfma_f32_16x16x32_bf16 v[22:25], v[94:97], v[204:207], v[22:25]
	v_mfma_f32_16x16x32_bf16 v[18:21], v[102:105], v[204:207], v[18:21]
	v_mfma_f32_16x16x32_bf16 v[14:17], v[94:97], v[216:219], v[14:17]
	v_mfma_f32_16x16x32_bf16 v[10:13], v[102:105], v[216:219], v[10:13]
	v_mfma_f32_16x16x32_bf16 v[6:9], v[94:97], v[224:227], v[6:9]
	v_mfma_f32_16x16x32_bf16 v[2:5], v[102:105], v[224:227], v[2:5]
	s_setprio 0
	s_setprio 1
	v_mfma_f32_16x16x32_bf16 v[86:89], v[146:149], v[200:203], 0
	v_mfma_f32_16x16x32_bf16 v[82:85], v[180:183], v[200:203], 0
	v_mfma_f32_16x16x32_bf16 v[78:81], v[146:149], v[208:211], 0
	v_mfma_f32_16x16x32_bf16 v[74:77], v[180:183], v[208:211], 0
	v_mfma_f32_16x16x32_bf16 v[62:65], v[146:149], v[220:223], 0
	v_mfma_f32_16x16x32_bf16 v[58:61], v[180:183], v[220:223], 0
	v_mfma_f32_16x16x32_bf16 v[90:93], v[146:149], v[188:191], 0
	v_mfma_f32_16x16x32_bf16 v[94:97], v[180:183], v[188:191], 0
	v_mfma_f32_16x16x32_bf16 v[86:89], v[150:153], v[204:207], v[86:89]
	v_mfma_f32_16x16x32_bf16 v[82:85], v[184:187], v[204:207], v[82:85]
	v_mfma_f32_16x16x32_bf16 v[78:81], v[150:153], v[216:219], v[78:81]
	v_mfma_f32_16x16x32_bf16 v[74:77], v[184:187], v[216:219], v[74:77]
	v_mfma_f32_16x16x32_bf16 v[62:65], v[150:153], v[224:227], v[62:65]
	v_mfma_f32_16x16x32_bf16 v[58:61], v[184:187], v[224:227], v[58:61]
	v_mfma_f32_16x16x32_bf16 v[90:93], v[150:153], v[192:195], v[90:93]
	v_mfma_f32_16x16x32_bf16 v[94:97], v[184:187], v[192:195], v[94:97]
	s_barrier
	s_setprio 0
	s_add_i32 s66, 0, 0x18000
	s_add_i32 s67, 0, 0x1c000
	v_add_u32_e32 v110, s66, v165
	v_add_u32_e32 v162, s67, v165
	ds_read_b128 v[98:101], v110
	ds_read_b128 v[102:105], v110 offset:1024
	ds_read_b128 v[106:109], v110 offset:2048
	ds_read_b128 v[110:113], v110 offset:3072
	ds_read_b128 v[146:149], v162
	ds_read_b128 v[150:153], v162 offset:1024
	ds_read_b128 v[180:183], v162 offset:2048
	ds_read_b128 v[184:187], v162 offset:3072
	s_add_u32 s38, s38, 0x80000
	s_addc_u32 s39, s39, 0
	s_mov_b32 m0, s47
	v_lshl_add_u64 v[232:233], s[38:39], 0, v[154:155]
	ds_read_b128 v[188:191], v199 offset:32768
	ds_read_b128 v[192:195], v199 offset:33792
	ds_read_b128 v[200:203], v199 offset:34816
	ds_read_b128 v[204:207], v199 offset:35840
	ds_read_b128 v[208:211], v199 offset:36864
	ds_read_b128 v[216:219], v199 offset:37888
	ds_read_b128 v[220:223], v199 offset:38912
	ds_read_b128 v[224:227], v199 offset:39936
	global_load_lds_dwordx4 v[232:233], off
	v_lshl_add_u64 v[232:233], s[38:39], 0, v[158:159]
	s_mov_b32 m0, s48
	s_nop 0
	global_load_lds_dwordx4 v[232:233], off
	s_waitcnt vmcnt(8)
	s_waitcnt lgkmcnt(0)
	s_setprio 1
	s_barrier
	v_mfma_f32_16x16x32_bf16 v[70:73], v[98:101], v[188:191], v[70:73]
	v_mfma_f32_16x16x32_bf16 v[66:69], v[106:109], v[188:191], v[66:69]
	v_mfma_f32_16x16x32_bf16 v[54:57], v[98:101], v[200:203], v[54:57]
	v_mfma_f32_16x16x32_bf16 v[50:53], v[106:109], v[200:203], v[50:53]
	v_mfma_f32_16x16x32_bf16 v[46:49], v[98:101], v[208:211], v[46:49]
	v_mfma_f32_16x16x32_bf16 v[42:45], v[106:109], v[208:211], v[42:45]
	v_mfma_f32_16x16x32_bf16 v[38:41], v[98:101], v[220:223], v[38:41]
	v_mfma_f32_16x16x32_bf16 v[34:37], v[106:109], v[220:223], v[34:37]
	v_mfma_f32_16x16x32_bf16 v[70:73], v[102:105], v[192:195], v[70:73]
	v_mfma_f32_16x16x32_bf16 v[66:69], v[110:113], v[192:195], v[66:69]
	v_mfma_f32_16x16x32_bf16 v[54:57], v[102:105], v[204:207], v[54:57]
	v_mfma_f32_16x16x32_bf16 v[50:53], v[110:113], v[204:207], v[50:53]
	v_mfma_f32_16x16x32_bf16 v[46:49], v[102:105], v[216:219], v[46:49]
	v_mfma_f32_16x16x32_bf16 v[42:45], v[110:113], v[216:219], v[42:45]
	v_mfma_f32_16x16x32_bf16 v[38:41], v[102:105], v[224:227], v[38:41]
	v_mfma_f32_16x16x32_bf16 v[34:37], v[110:113], v[224:227], v[34:37]
	s_setprio 0
	s_setprio 1
	v_mfma_f32_16x16x32_bf16 v[142:145], v[146:149], v[188:191], v[142:145]
	v_mfma_f32_16x16x32_bf16 v[138:141], v[180:183], v[188:191], v[138:141]
	v_mfma_f32_16x16x32_bf16 v[134:137], v[146:149], v[200:203], v[134:137]
	v_mfma_f32_16x16x32_bf16 v[130:133], v[180:183], v[200:203], v[130:133]
	v_mfma_f32_16x16x32_bf16 v[126:129], v[146:149], v[208:211], v[126:129]
	v_mfma_f32_16x16x32_bf16 v[122:125], v[180:183], v[208:211], v[122:125]
	v_mfma_f32_16x16x32_bf16 v[118:121], v[146:149], v[220:223], v[118:121]
	v_mfma_f32_16x16x32_bf16 v[114:117], v[180:183], v[220:223], v[114:117]
	v_mfma_f32_16x16x32_bf16 v[142:145], v[150:153], v[192:195], v[142:145]
	v_mfma_f32_16x16x32_bf16 v[138:141], v[184:187], v[192:195], v[138:141]
	v_mfma_f32_16x16x32_bf16 v[134:137], v[150:153], v[204:207], v[134:137]
	v_mfma_f32_16x16x32_bf16 v[130:133], v[184:187], v[204:207], v[130:133]
	v_mfma_f32_16x16x32_bf16 v[126:129], v[150:153], v[216:219], v[126:129]
	v_mfma_f32_16x16x32_bf16 v[122:125], v[184:187], v[216:219], v[122:125]
	v_mfma_f32_16x16x32_bf16 v[118:121], v[150:153], v[224:227], v[118:121]
	v_mfma_f32_16x16x32_bf16 v[114:117], v[184:187], v[224:227], v[114:117]
	s_barrier
	s_setprio 0
	s_add_i32 s38, s66, s43
	v_lshl_add_u64 v[212:213], v[212:213], 0, s[18:19]
	s_mov_b32 m0, s38
	ds_read_b128 v[188:191], v199 offset:49152
	ds_read_b128 v[192:195], v199 offset:50176
	ds_read_b128 v[200:203], v199 offset:51200
	ds_read_b128 v[204:207], v199 offset:52224
	ds_read_b128 v[208:211], v199 offset:53248
	ds_read_b128 v[216:219], v199 offset:54272
	ds_read_b128 v[220:223], v199 offset:55296
	ds_read_b128 v[224:227], v199 offset:56320
	global_load_lds_dwordx4 v[212:213], off
	s_add_i32 m0, s38, 0x2000
	s_add_u32 s36, s36, 0x80080
	v_lshl_add_u64 v[212:213], v[214:215], 0, s[18:19]
	s_addc_u32 s37, s37, 0
	s_add_i32 s38, s67, s43
	global_load_lds_dwordx4 v[212:213], off
	v_lshl_add_u64 v[212:213], s[36:37], 0, v[156:157]
	s_mov_b32 m0, s38
	s_nop 0
	global_load_lds_dwordx4 v[212:213], off
	v_lshl_add_u64 v[212:213], s[36:37], 0, v[160:161]
	s_add_i32 m0, s38, 0x2000
	s_nop 0
	global_load_lds_dwordx4 v[212:213], off
	v_lshl_add_u64 v[212:213], v[228:229], 0, s[18:19]
	s_mov_b32 m0, s52
	s_nop 0
	global_load_lds_dwordx4 v[212:213], off
	v_lshl_add_u64 v[212:213], v[230:231], 0, s[18:19]
	s_mov_b32 m0, s53
	s_nop 0
	global_load_lds_dwordx4 v[212:213], off
	s_waitcnt vmcnt(8)
	s_waitcnt lgkmcnt(0)
	s_setprio 1
	s_barrier
	v_mfma_f32_16x16x32_bf16 v[30:33], v[98:101], v[188:191], v[30:33]
	v_mfma_f32_16x16x32_bf16 v[26:29], v[106:109], v[188:191], v[26:29]
	v_mfma_f32_16x16x32_bf16 v[22:25], v[98:101], v[200:203], v[22:25]
	v_mfma_f32_16x16x32_bf16 v[18:21], v[106:109], v[200:203], v[18:21]
	v_mfma_f32_16x16x32_bf16 v[14:17], v[98:101], v[208:211], v[14:17]
	v_mfma_f32_16x16x32_bf16 v[10:13], v[106:109], v[208:211], v[10:13]
	v_mfma_f32_16x16x32_bf16 v[6:9], v[98:101], v[220:223], v[6:9]
	v_mfma_f32_16x16x32_bf16 v[2:5], v[106:109], v[220:223], v[2:5]
	v_mfma_f32_16x16x32_bf16 v[30:33], v[102:105], v[192:195], v[30:33]
	v_mfma_f32_16x16x32_bf16 v[26:29], v[110:113], v[192:195], v[26:29]
	v_mfma_f32_16x16x32_bf16 v[22:25], v[102:105], v[204:207], v[22:25]
	v_mfma_f32_16x16x32_bf16 v[18:21], v[110:113], v[204:207], v[18:21]
	v_mfma_f32_16x16x32_bf16 v[14:17], v[102:105], v[216:219], v[14:17]
	v_mfma_f32_16x16x32_bf16 v[10:13], v[110:113], v[216:219], v[10:13]
	v_mfma_f32_16x16x32_bf16 v[6:9], v[102:105], v[224:227], v[6:9]
	v_mfma_f32_16x16x32_bf16 v[2:5], v[110:113], v[224:227], v[2:5]
	s_setprio 0
	s_setprio 1
	v_mfma_f32_16x16x32_bf16 v[90:93], v[146:149], v[188:191], v[90:93]
	v_mfma_f32_16x16x32_bf16 v[110:113], v[150:153], v[192:195], v[90:93]
	v_mfma_f32_16x16x32_bf16 v[90:93], v[180:183], v[188:191], v[94:97]
	v_mfma_f32_16x16x32_bf16 v[86:89], v[146:149], v[200:203], v[86:89]
	v_mfma_f32_16x16x32_bf16 v[82:85], v[180:183], v[200:203], v[82:85]
	v_mfma_f32_16x16x32_bf16 v[78:81], v[146:149], v[208:211], v[78:81]
	v_mfma_f32_16x16x32_bf16 v[74:77], v[180:183], v[208:211], v[74:77]
	v_mfma_f32_16x16x32_bf16 v[62:65], v[146:149], v[220:223], v[62:65]
	v_mfma_f32_16x16x32_bf16 v[58:61], v[180:183], v[220:223], v[58:61]
	v_mfma_f32_16x16x32_bf16 v[106:109], v[184:187], v[192:195], v[90:93]
	v_mfma_f32_16x16x32_bf16 v[86:89], v[150:153], v[204:207], v[86:89]
	v_mfma_f32_16x16x32_bf16 v[82:85], v[184:187], v[204:207], v[82:85]
	v_mfma_f32_16x16x32_bf16 v[78:81], v[150:153], v[216:219], v[78:81]
	v_mfma_f32_16x16x32_bf16 v[74:77], v[184:187], v[216:219], v[74:77]
	v_mfma_f32_16x16x32_bf16 v[62:65], v[150:153], v[224:227], v[62:65]
	v_mfma_f32_16x16x32_bf16 v[58:61], v[184:187], v[224:227], v[58:61]
	s_barrier
	s_setprio 0
	s_add_i32 s65, s65, 2
	s_add_u32 s16, s16, 0x100
	s_addc_u32 s17, s17, 0
	s_add_u32 s41, s41, 0x100
	s_addc_u32 s64, s64, 0
	s_cmp_gt_u32 s65, 29
	.p2alignl 6, 3212836864

.LBB0_427:
	s_ashr_i32 s25, s24, 31
	s_lshl_b64 s[8:9], s[24:25], 20
	s_add_u32 s10, s86, s8
	s_addc_u32 s11, s87, s9
	s_and_b64 s[8:9], s[34:35], exec
	s_cselect_b32 s25, s11, s1
	s_cselect_b32 s55, s10, s0
	s_ashr_i32 s27, s26, 31
	s_lshl_b64 s[8:9], s[26:27], 20
	s_add_u32 s8, s86, s8
	s_addc_u32 s9, s87, s9
	s_and_b64 s[34:35], s[34:35], exec
	s_cselect_b32 s27, s9, s31
	s_cselect_b32 s56, s8, s30
	s_add_u32 s0, s0, 0x80080
	s_addc_u32 s1, s1, 0
	s_add_u32 s57, s30, 0x100
	s_addc_u32 s58, s31, 0
	s_mov_b32 s59, -2
	ds_read_b128 v[150:153], v146
	ds_read_b128 v[154:157], v146 offset:1024
	ds_read_b128 v[158:161], v146 offset:2048
	ds_read_b128 v[162:165], v146 offset:3072
	ds_read_b128 v[166:169], v147
	ds_read_b128 v[170:173], v147 offset:1024
	ds_read_b128 v[174:177], v147 offset:2048
	ds_read_b128 v[178:181], v147 offset:3072
	s_add_u32 s30, s0, 0xfff80080
	s_addc_u32 s31, s1, -1
	s_cmp_eq_u32 s59, 28
	s_cselect_b32 s35, s25, s31
	s_cselect_b32 s34, s55, s30
	s_cselect_b32 s31, s27, s58
	s_cselect_b32 s30, s56, s57
	v_lshl_add_u64 v[142:143], s[0:1], 0, v[138:139]
	s_add_i32 m0, s39, 0xc000
	ds_read_b128 v[182:185], v148
	ds_read_b128 v[186:189], v148 offset:1024
	ds_read_b128 v[190:193], v148 offset:2048
	ds_read_b128 v[194:197], v148 offset:3072
	ds_read_b128 v[198:201], v148 offset:4096
	ds_read_b128 v[202:205], v148 offset:5120
	ds_read_b128 v[206:209], v148 offset:6144
	ds_read_b128 v[210:213], v148 offset:7168
	global_load_lds_dwordx4 v[142:143], off
	v_lshl_add_u64 v[142:143], s[0:1], 0, v[140:141]
	s_add_i32 m0, s39, 0xe000
	s_nop 0
	global_load_lds_dwordx4 v[142:143], off
	s_waitcnt vmcnt(8)
	s_waitcnt lgkmcnt(0)
	s_setprio 1
	s_barrier
	v_mfma_f32_16x16x32_bf16 v[94:97], v[150:153], v[182:185], 0
	v_mfma_f32_16x16x32_bf16 v[86:89], v[158:161], v[182:185], 0
	v_mfma_f32_16x16x32_bf16 v[66:69], v[150:153], v[190:193], 0
	v_mfma_f32_16x16x32_bf16 v[50:53], v[158:161], v[190:193], 0
	v_mfma_f32_16x16x32_bf16 v[46:49], v[150:153], v[198:201], 0
	v_mfma_f32_16x16x32_bf16 v[42:45], v[158:161], v[198:201], 0
	v_mfma_f32_16x16x32_bf16 v[38:41], v[150:153], v[206:209], 0
	v_mfma_f32_16x16x32_bf16 v[34:37], v[158:161], v[206:209], 0
	v_mfma_f32_16x16x32_bf16 v[94:97], v[154:157], v[186:189], v[94:97]
	v_mfma_f32_16x16x32_bf16 v[86:89], v[162:165], v[186:189], v[86:89]
	v_mfma_f32_16x16x32_bf16 v[66:69], v[154:157], v[194:197], v[66:69]
	v_mfma_f32_16x16x32_bf16 v[50:53], v[162:165], v[194:197], v[50:53]
	v_mfma_f32_16x16x32_bf16 v[46:49], v[154:157], v[202:205], v[46:49]
	v_mfma_f32_16x16x32_bf16 v[42:45], v[162:165], v[202:205], v[42:45]
	v_mfma_f32_16x16x32_bf16 v[38:41], v[154:157], v[210:213], v[38:41]
	v_mfma_f32_16x16x32_bf16 v[34:37], v[162:165], v[210:213], v[34:37]
	s_setprio 0
	s_setprio 1
	v_mfma_f32_16x16x32_bf16 v[126:129], v[166:169], v[182:185], 0
	v_mfma_f32_16x16x32_bf16 v[122:125], v[174:177], v[182:185], 0
	v_mfma_f32_16x16x32_bf16 v[118:121], v[166:169], v[190:193], 0
	v_mfma_f32_16x16x32_bf16 v[114:117], v[174:177], v[190:193], 0
	v_mfma_f32_16x16x32_bf16 v[110:113], v[166:169], v[198:201], 0
	v_mfma_f32_16x16x32_bf16 v[106:109], v[174:177], v[198:201], 0
	v_mfma_f32_16x16x32_bf16 v[102:105], v[166:169], v[206:209], 0
	v_mfma_f32_16x16x32_bf16 v[98:101], v[174:177], v[206:209], 0
	v_mfma_f32_16x16x32_bf16 v[126:129], v[170:173], v[186:189], v[126:129]
	v_mfma_f32_16x16x32_bf16 v[122:125], v[178:181], v[186:189], v[122:125]
	v_mfma_f32_16x16x32_bf16 v[118:121], v[170:173], v[194:197], v[118:121]
	v_mfma_f32_16x16x32_bf16 v[114:117], v[178:181], v[194:197], v[114:117]
	v_mfma_f32_16x16x32_bf16 v[110:113], v[170:173], v[202:205], v[110:113]
	v_mfma_f32_16x16x32_bf16 v[106:109], v[178:181], v[202:205], v[106:109]
	v_mfma_f32_16x16x32_bf16 v[102:105], v[170:173], v[210:213], v[102:105]
	v_mfma_f32_16x16x32_bf16 v[98:101], v[178:181], v[210:213], v[98:101]
	s_barrier
	s_setprio 0
	s_add_i32 s60, s47, s38
	v_lshl_add_u64 v[142:143], s[30:31], 0, v[130:131]
	s_mov_b32 m0, s60
	ds_read_b128 v[182:185], v148 offset:16384
	ds_read_b128 v[186:189], v148 offset:17408
	ds_read_b128 v[190:193], v148 offset:18432
	ds_read_b128 v[194:197], v148 offset:19456
	ds_read_b128 v[198:201], v148 offset:20480
	ds_read_b128 v[202:205], v148 offset:21504
	ds_read_b128 v[206:209], v148 offset:22528
	ds_read_b128 v[210:213], v148 offset:23552
	global_load_lds_dwordx4 v[142:143], off
	s_add_i32 m0, s60, 0x2000
	s_add_u32 s60, s30, 0x80000
	v_lshl_add_u64 v[214:215], s[30:31], 0, v[132:133]
	s_addc_u32 s61, s31, 0
	s_add_i32 s62, s48, s38
	global_load_lds_dwordx4 v[214:215], off
	v_lshl_add_u64 v[216:217], s[60:61], 0, v[130:131]
	s_mov_b32 m0, s62
	v_lshl_add_u64 v[218:219], s[34:35], 0, v[132:133]
	global_load_lds_dwordx4 v[216:217], off
	v_lshl_add_u64 v[216:217], s[60:61], 0, v[132:133]
	s_add_i32 m0, s62, 0x2000
	s_nop 0
	global_load_lds_dwordx4 v[216:217], off
	v_lshl_add_u64 v[216:217], s[34:35], 0, v[130:131]
	s_mov_b32 m0, s39
	s_nop 0
	global_load_lds_dwordx4 v[216:217], off
	s_mov_b32 m0, s40
	s_nop 0
	global_load_lds_dwordx4 v[218:219], off
	s_waitcnt vmcnt(8)
	s_waitcnt lgkmcnt(0)
	s_setprio 1
	s_barrier
	v_mfma_f32_16x16x32_bf16 v[30:33], v[150:153], v[182:185], 0
	v_mfma_f32_16x16x32_bf16 v[26:29], v[158:161], v[182:185], 0
	v_mfma_f32_16x16x32_bf16 v[22:25], v[150:153], v[190:193], 0
	v_mfma_f32_16x16x32_bf16 v[18:21], v[158:161], v[190:193], 0
	v_mfma_f32_16x16x32_bf16 v[14:17], v[150:153], v[198:201], 0
	v_mfma_f32_16x16x32_bf16 v[10:13], v[158:161], v[198:201], 0
	v_mfma_f32_16x16x32_bf16 v[6:9], v[150:153], v[206:209], 0
	v_mfma_f32_16x16x32_bf16 v[2:5], v[158:161], v[206:209], 0
	v_mfma_f32_16x16x32_bf16 v[30:33], v[154:157], v[186:189], v[30:33]
	v_mfma_f32_16x16x32_bf16 v[26:29], v[162:165], v[186:189], v[26:29]
	v_mfma_f32_16x16x32_bf16 v[22:25], v[154:157], v[194:197], v[22:25]
	v_mfma_f32_16x16x32_bf16 v[18:21], v[162:165], v[194:197], v[18:21]
	v_mfma_f32_16x16x32_bf16 v[14:17], v[154:157], v[202:205], v[14:17]
	v_mfma_f32_16x16x32_bf16 v[10:13], v[162:165], v[202:205], v[10:13]
	v_mfma_f32_16x16x32_bf16 v[6:9], v[154:157], v[210:213], v[6:9]
	v_mfma_f32_16x16x32_bf16 v[2:5], v[162:165], v[210:213], v[2:5]
	s_setprio 0
	s_setprio 1
	v_mfma_f32_16x16x32_bf16 v[90:93], v[166:169], v[182:185], 0
	v_mfma_f32_16x16x32_bf16 v[82:85], v[174:177], v[182:185], 0
	v_mfma_f32_16x16x32_bf16 v[78:81], v[166:169], v[190:193], 0
	v_mfma_f32_16x16x32_bf16 v[74:77], v[174:177], v[190:193], 0
	v_mfma_f32_16x16x32_bf16 v[70:73], v[166:169], v[198:201], 0
	v_mfma_f32_16x16x32_bf16 v[62:65], v[174:177], v[198:201], 0
	v_mfma_f32_16x16x32_bf16 v[58:61], v[166:169], v[206:209], 0
	v_mfma_f32_16x16x32_bf16 v[54:57], v[174:177], v[206:209], 0
	v_mfma_f32_16x16x32_bf16 v[90:93], v[170:173], v[186:189], v[90:93]
	v_mfma_f32_16x16x32_bf16 v[82:85], v[178:181], v[186:189], v[82:85]
	v_mfma_f32_16x16x32_bf16 v[78:81], v[170:173], v[194:197], v[78:81]
	v_mfma_f32_16x16x32_bf16 v[74:77], v[178:181], v[194:197], v[74:77]
	v_mfma_f32_16x16x32_bf16 v[70:73], v[170:173], v[202:205], v[70:73]
	v_mfma_f32_16x16x32_bf16 v[62:65], v[178:181], v[202:205], v[62:65]
	v_mfma_f32_16x16x32_bf16 v[58:61], v[170:173], v[210:213], v[58:61]
	v_mfma_f32_16x16x32_bf16 v[54:57], v[178:181], v[210:213], v[54:57]
	s_barrier
	s_setprio 0
	s_add_i32 s60, 0, 0x18000
	v_add_u32_e32 v134, s60, v144
	s_add_i32 s61, 0, 0x1c000
	ds_read_b128 v[150:153], v134
	ds_read_b128 v[154:157], v134 offset:1024
	ds_read_b128 v[158:161], v134 offset:2048
	ds_read_b128 v[162:165], v134 offset:3072
	v_add_u32_e32 v134, s61, v144
	ds_read_b128 v[166:169], v134
	ds_read_b128 v[170:173], v134 offset:1024
	ds_read_b128 v[174:177], v134 offset:2048
	ds_read_b128 v[178:181], v134 offset:3072
	s_add_u32 s34, s34, 0x80000
	s_addc_u32 s35, s35, 0
	s_mov_b32 m0, s41
	v_lshl_add_u64 v[220:221], s[34:35], 0, v[130:131]
	ds_read_b128 v[182:185], v148 offset:32768
	ds_read_b128 v[186:189], v148 offset:33792
	ds_read_b128 v[190:193], v148 offset:34816
	ds_read_b128 v[194:197], v148 offset:35840
	ds_read_b128 v[198:201], v148 offset:36864
	ds_read_b128 v[202:205], v148 offset:37888
	ds_read_b128 v[206:209], v148 offset:38912
	ds_read_b128 v[210:213], v148 offset:39936
	global_load_lds_dwordx4 v[220:221], off
	v_lshl_add_u64 v[220:221], s[34:35], 0, v[132:133]
	s_mov_b32 m0, s42
	s_nop 0
	global_load_lds_dwordx4 v[220:221], off
	s_waitcnt vmcnt(8)
	s_waitcnt lgkmcnt(0)
	s_setprio 1
	s_barrier
	v_mfma_f32_16x16x32_bf16 v[94:97], v[150:153], v[182:185], v[94:97]
	v_mfma_f32_16x16x32_bf16 v[86:89], v[158:161], v[182:185], v[86:89]
	v_mfma_f32_16x16x32_bf16 v[66:69], v[150:153], v[190:193], v[66:69]
	v_mfma_f32_16x16x32_bf16 v[50:53], v[158:161], v[190:193], v[50:53]
	v_mfma_f32_16x16x32_bf16 v[46:49], v[150:153], v[198:201], v[46:49]
	v_mfma_f32_16x16x32_bf16 v[42:45], v[158:161], v[198:201], v[42:45]
	v_mfma_f32_16x16x32_bf16 v[38:41], v[150:153], v[206:209], v[38:41]
	v_mfma_f32_16x16x32_bf16 v[34:37], v[158:161], v[206:209], v[34:37]
	v_mfma_f32_16x16x32_bf16 v[94:97], v[154:157], v[186:189], v[94:97]
	v_mfma_f32_16x16x32_bf16 v[86:89], v[162:165], v[186:189], v[86:89]
	v_mfma_f32_16x16x32_bf16 v[66:69], v[154:157], v[194:197], v[66:69]
	v_mfma_f32_16x16x32_bf16 v[50:53], v[162:165], v[194:197], v[50:53]
	v_mfma_f32_16x16x32_bf16 v[46:49], v[154:157], v[202:205], v[46:49]
	v_mfma_f32_16x16x32_bf16 v[42:45], v[162:165], v[202:205], v[42:45]
	v_mfma_f32_16x16x32_bf16 v[38:41], v[154:157], v[210:213], v[38:41]
	v_mfma_f32_16x16x32_bf16 v[34:37], v[162:165], v[210:213], v[34:37]
	s_setprio 0
	s_setprio 1
	v_mfma_f32_16x16x32_bf16 v[126:129], v[166:169], v[182:185], v[126:129]
	v_mfma_f32_16x16x32_bf16 v[122:125], v[174:177], v[182:185], v[122:125]
	v_mfma_f32_16x16x32_bf16 v[118:121], v[166:169], v[190:193], v[118:121]
	v_mfma_f32_16x16x32_bf16 v[114:117], v[174:177], v[190:193], v[114:117]
	v_mfma_f32_16x16x32_bf16 v[110:113], v[166:169], v[198:201], v[110:113]
	v_mfma_f32_16x16x32_bf16 v[106:109], v[174:177], v[198:201], v[106:109]
	v_mfma_f32_16x16x32_bf16 v[102:105], v[166:169], v[206:209], v[102:105]
	v_mfma_f32_16x16x32_bf16 v[98:101], v[174:177], v[206:209], v[98:101]
	v_mfma_f32_16x16x32_bf16 v[126:129], v[170:173], v[186:189], v[126:129]
	v_mfma_f32_16x16x32_bf16 v[122:125], v[178:181], v[186:189], v[122:125]
	v_mfma_f32_16x16x32_bf16 v[118:121], v[170:173], v[194:197], v[118:121]
	v_mfma_f32_16x16x32_bf16 v[114:117], v[178:181], v[194:197], v[114:117]
	v_mfma_f32_16x16x32_bf16 v[110:113], v[170:173], v[202:205], v[110:113]
	v_mfma_f32_16x16x32_bf16 v[106:109], v[178:181], v[202:205], v[106:109]
	v_mfma_f32_16x16x32_bf16 v[102:105], v[170:173], v[210:213], v[102:105]
	v_mfma_f32_16x16x32_bf16 v[98:101], v[178:181], v[210:213], v[98:101]
	s_barrier
	s_setprio 0
	s_add_i32 s34, s60, s38
	v_lshl_add_u64 v[142:143], v[142:143], 0, s[6:7]
	s_mov_b32 m0, s34
	ds_read_b128 v[182:185], v148 offset:49152
	ds_read_b128 v[186:189], v148 offset:50176
	ds_read_b128 v[190:193], v148 offset:51200
	ds_read_b128 v[194:197], v148 offset:52224
	ds_read_b128 v[198:201], v148 offset:53248
	ds_read_b128 v[202:205], v148 offset:54272
	ds_read_b128 v[206:209], v148 offset:55296
	ds_read_b128 v[210:213], v148 offset:56320
	global_load_lds_dwordx4 v[142:143], off
	s_add_i32 m0, s34, 0x2000
	s_add_u32 s30, s30, 0x80080
	v_lshl_add_u64 v[142:143], v[214:215], 0, s[6:7]
	s_addc_u32 s31, s31, 0
	s_add_i32 s34, s61, s38
	global_load_lds_dwordx4 v[142:143], off
	v_lshl_add_u64 v[142:143], s[30:31], 0, v[130:131]
	s_mov_b32 m0, s34
	s_nop 0
	global_load_lds_dwordx4 v[142:143], off
	v_lshl_add_u64 v[142:143], s[30:31], 0, v[132:133]
	s_add_i32 m0, s34, 0x2000
	s_nop 0
	global_load_lds_dwordx4 v[142:143], off
	v_lshl_add_u64 v[142:143], v[216:217], 0, s[6:7]
	s_mov_b32 m0, s44
	s_nop 0
	global_load_lds_dwordx4 v[142:143], off
	v_lshl_add_u64 v[142:143], v[218:219], 0, s[6:7]
	s_mov_b32 m0, s45
	s_nop 0
	global_load_lds_dwordx4 v[142:143], off
	s_waitcnt vmcnt(8)
	s_waitcnt lgkmcnt(0)
	s_setprio 1
	s_barrier
	v_mfma_f32_16x16x32_bf16 v[30:33], v[150:153], v[182:185], v[30:33]
	v_mfma_f32_16x16x32_bf16 v[26:29], v[158:161], v[182:185], v[26:29]
	v_mfma_f32_16x16x32_bf16 v[22:25], v[150:153], v[190:193], v[22:25]
	v_mfma_f32_16x16x32_bf16 v[18:21], v[158:161], v[190:193], v[18:21]
	v_mfma_f32_16x16x32_bf16 v[14:17], v[150:153], v[198:201], v[14:17]
	v_mfma_f32_16x16x32_bf16 v[10:13], v[158:161], v[198:201], v[10:13]
	v_mfma_f32_16x16x32_bf16 v[6:9], v[150:153], v[206:209], v[6:9]
	v_mfma_f32_16x16x32_bf16 v[2:5], v[158:161], v[206:209], v[2:5]
	v_mfma_f32_16x16x32_bf16 v[30:33], v[154:157], v[186:189], v[30:33]
	v_mfma_f32_16x16x32_bf16 v[26:29], v[162:165], v[186:189], v[26:29]
	v_mfma_f32_16x16x32_bf16 v[22:25], v[154:157], v[194:197], v[22:25]
	v_mfma_f32_16x16x32_bf16 v[18:21], v[162:165], v[194:197], v[18:21]
	v_mfma_f32_16x16x32_bf16 v[14:17], v[154:157], v[202:205], v[14:17]
	v_mfma_f32_16x16x32_bf16 v[10:13], v[162:165], v[202:205], v[10:13]
	v_mfma_f32_16x16x32_bf16 v[6:9], v[154:157], v[210:213], v[6:9]
	v_mfma_f32_16x16x32_bf16 v[2:5], v[162:165], v[210:213], v[2:5]
	s_setprio 0
	s_setprio 1
	v_mfma_f32_16x16x32_bf16 v[90:93], v[166:169], v[182:185], v[90:93]
	v_mfma_f32_16x16x32_bf16 v[82:85], v[174:177], v[182:185], v[82:85]
	v_mfma_f32_16x16x32_bf16 v[78:81], v[166:169], v[190:193], v[78:81]
	v_mfma_f32_16x16x32_bf16 v[74:77], v[174:177], v[190:193], v[74:77]
	v_mfma_f32_16x16x32_bf16 v[70:73], v[166:169], v[198:201], v[70:73]
	v_mfma_f32_16x16x32_bf16 v[62:65], v[174:177], v[198:201], v[62:65]
	v_mfma_f32_16x16x32_bf16 v[58:61], v[166:169], v[206:209], v[58:61]
	v_mfma_f32_16x16x32_bf16 v[54:57], v[174:177], v[206:209], v[54:57]
	v_mfma_f32_16x16x32_bf16 v[90:93], v[170:173], v[186:189], v[90:93]
	v_mfma_f32_16x16x32_bf16 v[82:85], v[178:181], v[186:189], v[82:85]
	v_mfma_f32_16x16x32_bf16 v[78:81], v[170:173], v[194:197], v[78:81]
	v_mfma_f32_16x16x32_bf16 v[74:77], v[178:181], v[194:197], v[74:77]
	v_mfma_f32_16x16x32_bf16 v[70:73], v[170:173], v[202:205], v[70:73]
	v_mfma_f32_16x16x32_bf16 v[62:65], v[178:181], v[202:205], v[62:65]
	v_mfma_f32_16x16x32_bf16 v[58:61], v[170:173], v[210:213], v[58:61]
	v_mfma_f32_16x16x32_bf16 v[54:57], v[178:181], v[210:213], v[54:57]
	s_barrier
	s_setprio 0
	s_add_i32 s59, s59, 2
	s_add_u32 s0, s0, 0x100
	s_addc_u32 s1, s1, 0
	s_add_u32 s57, s57, 0x100
	s_addc_u32 s58, s58, 0
	s_cmp_gt_u32 s59, 29
	.p2alignl 6, 3212836864

.LBB0_1345:
	s_ashr_i32 s23, s22, 31
	s_lshl_b64 s[24:25], s[22:23], 20
	v_readlane_b32 s26, v254, 22
	v_readlane_b32 s27, v254, 23
	s_add_u32 s24, s26, s24
	s_addc_u32 s25, s27, s25
	s_and_b64 s[26:27], s[8:9], exec
	s_cselect_b32 s23, s25, s31
	s_cselect_b32 s55, s24, s30
	s_ashr_i32 s21, s20, 31
	s_lshl_b64 s[26:27], s[20:21], 20
	s_add_u32 s26, s38, s26
	s_addc_u32 s27, s39, s27
	s_and_b64 s[36:37], s[8:9], exec
	s_cselect_b32 s21, s27, s35
	s_cselect_b32 s56, s26, s34
	s_add_u32 s30, s30, 0x80080
	s_addc_u32 s31, s31, 0
	s_add_u32 s57, s34, 0x100
	s_addc_u32 s58, s35, 0
	s_mov_b32 s59, -2
	ds_read_b128 v[154:157], v150
	ds_read_b128 v[158:161], v150 offset:1024
	ds_read_b128 v[162:165], v150 offset:2048
	ds_read_b128 v[166:169], v150 offset:3072
	ds_read_b128 v[170:173], v151
	ds_read_b128 v[174:177], v151 offset:1024
	ds_read_b128 v[178:181], v151 offset:2048
	ds_read_b128 v[182:185], v151 offset:3072
	s_add_u32 s34, s30, 0xfff80080
	s_addc_u32 s35, s31, -1
	s_cmp_eq_u32 s59, 28
	s_cselect_b32 s37, s23, s35
	s_cselect_b32 s36, s55, s34
	s_cselect_b32 s35, s21, s58
	s_cselect_b32 s34, s56, s57
	v_lshl_add_u64 v[146:147], s[30:31], 0, v[138:139]
	s_add_i32 m0, s29, 0xc000
	ds_read_b128 v[186:189], v152
	ds_read_b128 v[190:193], v152 offset:1024
	ds_read_b128 v[194:197], v152 offset:2048
	ds_read_b128 v[198:201], v152 offset:3072
	ds_read_b128 v[202:205], v152 offset:4096
	ds_read_b128 v[206:209], v152 offset:5120
	ds_read_b128 v[210:213], v152 offset:6144
	ds_read_b128 v[214:217], v152 offset:7168
	global_load_lds_dwordx4 v[146:147], off
	v_lshl_add_u64 v[146:147], s[30:31], 0, v[140:141]
	s_add_i32 m0, s29, 0xe000
	s_nop 0
	global_load_lds_dwordx4 v[146:147], off
	s_waitcnt vmcnt(8)
	s_waitcnt lgkmcnt(0)
	s_setprio 1
	s_barrier
	v_mfma_f32_16x16x32_bf16 v[126:129], v[154:157], v[186:189], 0
	v_mfma_f32_16x16x32_bf16 v[122:125], v[162:165], v[186:189], 0
	v_mfma_f32_16x16x32_bf16 v[118:121], v[154:157], v[194:197], 0
	v_mfma_f32_16x16x32_bf16 v[110:113], v[162:165], v[194:197], 0
	v_mfma_f32_16x16x32_bf16 v[102:105], v[154:157], v[202:205], 0
	v_mfma_f32_16x16x32_bf16 v[94:97], v[162:165], v[202:205], 0
	v_mfma_f32_16x16x32_bf16 v[86:89], v[154:157], v[210:213], 0
	v_mfma_f32_16x16x32_bf16 v[78:81], v[162:165], v[210:213], 0
	v_mfma_f32_16x16x32_bf16 v[126:129], v[158:161], v[190:193], v[126:129]
	v_mfma_f32_16x16x32_bf16 v[122:125], v[166:169], v[190:193], v[122:125]
	v_mfma_f32_16x16x32_bf16 v[118:121], v[158:161], v[198:201], v[118:121]
	v_mfma_f32_16x16x32_bf16 v[110:113], v[166:169], v[198:201], v[110:113]
	v_mfma_f32_16x16x32_bf16 v[102:105], v[158:161], v[206:209], v[102:105]
	v_mfma_f32_16x16x32_bf16 v[94:97], v[166:169], v[206:209], v[94:97]
	v_mfma_f32_16x16x32_bf16 v[86:89], v[158:161], v[214:217], v[86:89]
	v_mfma_f32_16x16x32_bf16 v[78:81], v[166:169], v[214:217], v[78:81]
	s_setprio 0
	s_setprio 1
	v_mfma_f32_16x16x32_bf16 v[114:117], v[170:173], v[186:189], 0
	v_mfma_f32_16x16x32_bf16 v[106:109], v[178:181], v[186:189], 0
	v_mfma_f32_16x16x32_bf16 v[98:101], v[170:173], v[194:197], 0
	v_mfma_f32_16x16x32_bf16 v[90:93], v[178:181], v[194:197], 0
	v_mfma_f32_16x16x32_bf16 v[82:85], v[170:173], v[202:205], 0
	v_mfma_f32_16x16x32_bf16 v[74:77], v[178:181], v[202:205], 0
	v_mfma_f32_16x16x32_bf16 v[70:73], v[170:173], v[210:213], 0
	v_mfma_f32_16x16x32_bf16 v[66:69], v[178:181], v[210:213], 0
	v_mfma_f32_16x16x32_bf16 v[114:117], v[174:177], v[190:193], v[114:117]
	v_mfma_f32_16x16x32_bf16 v[106:109], v[182:185], v[190:193], v[106:109]
	v_mfma_f32_16x16x32_bf16 v[98:101], v[174:177], v[198:201], v[98:101]
	v_mfma_f32_16x16x32_bf16 v[90:93], v[182:185], v[198:201], v[90:93]
	v_mfma_f32_16x16x32_bf16 v[82:85], v[174:177], v[206:209], v[82:85]
	v_mfma_f32_16x16x32_bf16 v[74:77], v[182:185], v[206:209], v[74:77]
	v_mfma_f32_16x16x32_bf16 v[70:73], v[174:177], v[214:217], v[70:73]
	v_mfma_f32_16x16x32_bf16 v[66:69], v[182:185], v[214:217], v[66:69]
	s_barrier
	s_setprio 0
	s_add_i32 s60, s48, s40
	v_lshl_add_u64 v[146:147], s[34:35], 0, v[132:133]
	s_mov_b32 m0, s60
	ds_read_b128 v[186:189], v152 offset:16384
	ds_read_b128 v[190:193], v152 offset:17408
	ds_read_b128 v[194:197], v152 offset:18432
	ds_read_b128 v[198:201], v152 offset:19456
	ds_read_b128 v[202:205], v152 offset:20480
	ds_read_b128 v[206:209], v152 offset:21504
	ds_read_b128 v[210:213], v152 offset:22528
	ds_read_b128 v[214:217], v152 offset:23552
	global_load_lds_dwordx4 v[146:147], off
	s_add_i32 m0, s60, 0x2000
	s_add_u32 s60, s34, 0x80000
	v_lshl_add_u64 v[218:219], s[34:35], 0, v[136:137]
	s_addc_u32 s61, s35, 0
	s_add_i32 s62, s49, s40
	global_load_lds_dwordx4 v[218:219], off
	v_lshl_add_u64 v[220:221], s[60:61], 0, v[132:133]
	s_mov_b32 m0, s62
	v_lshl_add_u64 v[222:223], s[36:37], 0, v[134:135]
	global_load_lds_dwordx4 v[220:221], off
	v_lshl_add_u64 v[220:221], s[60:61], 0, v[136:137]
	s_add_i32 m0, s62, 0x2000
	s_nop 0
	global_load_lds_dwordx4 v[220:221], off
	v_lshl_add_u64 v[220:221], s[36:37], 0, v[130:131]
	s_mov_b32 m0, s29
	s_nop 0
	global_load_lds_dwordx4 v[220:221], off
	s_mov_b32 m0, s41
	s_nop 0
	global_load_lds_dwordx4 v[222:223], off
	s_waitcnt vmcnt(8)
	s_waitcnt lgkmcnt(0)
	s_setprio 1
	s_barrier
	v_mfma_f32_16x16x32_bf16 v[62:65], v[154:157], v[186:189], 0
	v_mfma_f32_16x16x32_bf16 v[58:61], v[162:165], v[186:189], 0
	v_mfma_f32_16x16x32_bf16 v[54:57], v[154:157], v[194:197], 0
	v_mfma_f32_16x16x32_bf16 v[46:49], v[162:165], v[194:197], 0
	v_mfma_f32_16x16x32_bf16 v[38:41], v[154:157], v[202:205], 0
	v_mfma_f32_16x16x32_bf16 v[30:33], v[162:165], v[202:205], 0
	v_mfma_f32_16x16x32_bf16 v[22:25], v[154:157], v[210:213], 0
	v_mfma_f32_16x16x32_bf16 v[14:17], v[162:165], v[210:213], 0
	v_mfma_f32_16x16x32_bf16 v[62:65], v[158:161], v[190:193], v[62:65]
	v_mfma_f32_16x16x32_bf16 v[58:61], v[166:169], v[190:193], v[58:61]
	v_mfma_f32_16x16x32_bf16 v[54:57], v[158:161], v[198:201], v[54:57]
	v_mfma_f32_16x16x32_bf16 v[46:49], v[166:169], v[198:201], v[46:49]
	v_mfma_f32_16x16x32_bf16 v[38:41], v[158:161], v[206:209], v[38:41]
	v_mfma_f32_16x16x32_bf16 v[30:33], v[166:169], v[206:209], v[30:33]
	v_mfma_f32_16x16x32_bf16 v[22:25], v[158:161], v[214:217], v[22:25]
	v_mfma_f32_16x16x32_bf16 v[14:17], v[166:169], v[214:217], v[14:17]
	s_setprio 0
	s_setprio 1
	v_mfma_f32_16x16x32_bf16 v[50:53], v[170:173], v[186:189], 0
	v_mfma_f32_16x16x32_bf16 v[42:45], v[178:181], v[186:189], 0
	v_mfma_f32_16x16x32_bf16 v[34:37], v[170:173], v[194:197], 0
	v_mfma_f32_16x16x32_bf16 v[26:29], v[178:181], v[194:197], 0
	v_mfma_f32_16x16x32_bf16 v[18:21], v[170:173], v[202:205], 0
	v_mfma_f32_16x16x32_bf16 v[10:13], v[178:181], v[202:205], 0
	v_mfma_f32_16x16x32_bf16 v[6:9], v[170:173], v[210:213], 0
	v_mfma_f32_16x16x32_bf16 v[2:5], v[178:181], v[210:213], 0
	v_mfma_f32_16x16x32_bf16 v[50:53], v[174:177], v[190:193], v[50:53]
	v_mfma_f32_16x16x32_bf16 v[42:45], v[182:185], v[190:193], v[42:45]
	v_mfma_f32_16x16x32_bf16 v[34:37], v[174:177], v[198:201], v[34:37]
	v_mfma_f32_16x16x32_bf16 v[26:29], v[182:185], v[198:201], v[26:29]
	v_mfma_f32_16x16x32_bf16 v[18:21], v[174:177], v[206:209], v[18:21]
	v_mfma_f32_16x16x32_bf16 v[10:13], v[182:185], v[206:209], v[10:13]
	v_mfma_f32_16x16x32_bf16 v[6:9], v[174:177], v[214:217], v[6:9]
	v_mfma_f32_16x16x32_bf16 v[2:5], v[182:185], v[214:217], v[2:5]
	s_barrier
	s_setprio 0
	s_add_i32 s60, 0, 0x18000
	v_add_u32_e32 v153, s60, v148
	s_add_i32 s61, 0, 0x1c000
	ds_read_b128 v[154:157], v153
	ds_read_b128 v[158:161], v153 offset:1024
	ds_read_b128 v[162:165], v153 offset:2048
	ds_read_b128 v[166:169], v153 offset:3072
	v_add_u32_e32 v153, s61, v148
	ds_read_b128 v[170:173], v153
	ds_read_b128 v[174:177], v153 offset:1024
	ds_read_b128 v[178:181], v153 offset:2048
	ds_read_b128 v[182:185], v153 offset:3072
	s_add_u32 s36, s36, 0x80000
	s_addc_u32 s37, s37, 0
	s_mov_b32 m0, s42
	v_lshl_add_u64 v[224:225], s[36:37], 0, v[130:131]
	ds_read_b128 v[186:189], v152 offset:32768
	ds_read_b128 v[190:193], v152 offset:33792
	ds_read_b128 v[194:197], v152 offset:34816
	ds_read_b128 v[198:201], v152 offset:35840
	ds_read_b128 v[202:205], v152 offset:36864
	ds_read_b128 v[206:209], v152 offset:37888
	ds_read_b128 v[210:213], v152 offset:38912
	ds_read_b128 v[214:217], v152 offset:39936
	global_load_lds_dwordx4 v[224:225], off
	v_lshl_add_u64 v[224:225], s[36:37], 0, v[134:135]
	s_mov_b32 m0, s43
	s_nop 0
	global_load_lds_dwordx4 v[224:225], off
	s_waitcnt vmcnt(8)
	s_waitcnt lgkmcnt(0)
	s_setprio 1
	s_barrier
	v_mfma_f32_16x16x32_bf16 v[126:129], v[154:157], v[186:189], v[126:129]
	v_mfma_f32_16x16x32_bf16 v[122:125], v[162:165], v[186:189], v[122:125]
	v_mfma_f32_16x16x32_bf16 v[118:121], v[154:157], v[194:197], v[118:121]
	v_mfma_f32_16x16x32_bf16 v[110:113], v[162:165], v[194:197], v[110:113]
	v_mfma_f32_16x16x32_bf16 v[102:105], v[154:157], v[202:205], v[102:105]
	v_mfma_f32_16x16x32_bf16 v[94:97], v[162:165], v[202:205], v[94:97]
	v_mfma_f32_16x16x32_bf16 v[86:89], v[154:157], v[210:213], v[86:89]
	v_mfma_f32_16x16x32_bf16 v[78:81], v[162:165], v[210:213], v[78:81]
	v_mfma_f32_16x16x32_bf16 v[126:129], v[158:161], v[190:193], v[126:129]
	v_mfma_f32_16x16x32_bf16 v[122:125], v[166:169], v[190:193], v[122:125]
	v_mfma_f32_16x16x32_bf16 v[118:121], v[158:161], v[198:201], v[118:121]
	v_mfma_f32_16x16x32_bf16 v[110:113], v[166:169], v[198:201], v[110:113]
	v_mfma_f32_16x16x32_bf16 v[102:105], v[158:161], v[206:209], v[102:105]
	v_mfma_f32_16x16x32_bf16 v[94:97], v[166:169], v[206:209], v[94:97]
	v_mfma_f32_16x16x32_bf16 v[86:89], v[158:161], v[214:217], v[86:89]
	v_mfma_f32_16x16x32_bf16 v[78:81], v[166:169], v[214:217], v[78:81]
	s_setprio 0
	s_setprio 1
	v_mfma_f32_16x16x32_bf16 v[114:117], v[170:173], v[186:189], v[114:117]
	v_mfma_f32_16x16x32_bf16 v[106:109], v[178:181], v[186:189], v[106:109]
	v_mfma_f32_16x16x32_bf16 v[98:101], v[170:173], v[194:197], v[98:101]
	v_mfma_f32_16x16x32_bf16 v[90:93], v[178:181], v[194:197], v[90:93]
	v_mfma_f32_16x16x32_bf16 v[82:85], v[170:173], v[202:205], v[82:85]
	v_mfma_f32_16x16x32_bf16 v[74:77], v[178:181], v[202:205], v[74:77]
	v_mfma_f32_16x16x32_bf16 v[70:73], v[170:173], v[210:213], v[70:73]
	v_mfma_f32_16x16x32_bf16 v[66:69], v[178:181], v[210:213], v[66:69]
	v_mfma_f32_16x16x32_bf16 v[114:117], v[174:177], v[190:193], v[114:117]
	v_mfma_f32_16x16x32_bf16 v[106:109], v[182:185], v[190:193], v[106:109]
	v_mfma_f32_16x16x32_bf16 v[98:101], v[174:177], v[198:201], v[98:101]
	v_mfma_f32_16x16x32_bf16 v[90:93], v[182:185], v[198:201], v[90:93]
	v_mfma_f32_16x16x32_bf16 v[82:85], v[174:177], v[206:209], v[82:85]
	v_mfma_f32_16x16x32_bf16 v[74:77], v[182:185], v[206:209], v[74:77]
	v_mfma_f32_16x16x32_bf16 v[70:73], v[174:177], v[214:217], v[70:73]
	v_mfma_f32_16x16x32_bf16 v[66:69], v[182:185], v[214:217], v[66:69]
	s_barrier
	s_setprio 0
	s_add_i32 s36, s60, s40
	v_lshl_add_u64 v[146:147], v[146:147], 0, s[10:11]
	s_mov_b32 m0, s36
	ds_read_b128 v[186:189], v152 offset:49152
	ds_read_b128 v[190:193], v152 offset:50176
	ds_read_b128 v[194:197], v152 offset:51200
	ds_read_b128 v[198:201], v152 offset:52224
	ds_read_b128 v[202:205], v152 offset:53248
	ds_read_b128 v[206:209], v152 offset:54272
	ds_read_b128 v[210:213], v152 offset:55296
	ds_read_b128 v[214:217], v152 offset:56320
	global_load_lds_dwordx4 v[146:147], off
	s_add_i32 m0, s36, 0x2000
	s_add_u32 s34, s34, 0x80080
	v_lshl_add_u64 v[146:147], v[218:219], 0, s[10:11]
	s_addc_u32 s35, s35, 0
	s_add_i32 s36, s61, s40
	global_load_lds_dwordx4 v[146:147], off
	v_lshl_add_u64 v[146:147], s[34:35], 0, v[132:133]
	s_mov_b32 m0, s36
	s_nop 0
	global_load_lds_dwordx4 v[146:147], off
	v_lshl_add_u64 v[146:147], s[34:35], 0, v[136:137]
	s_add_i32 m0, s36, 0x2000
	s_nop 0
	global_load_lds_dwordx4 v[146:147], off
	v_lshl_add_u64 v[146:147], v[220:221], 0, s[10:11]
	s_mov_b32 m0, s45
	s_nop 0
	global_load_lds_dwordx4 v[146:147], off
	v_lshl_add_u64 v[146:147], v[222:223], 0, s[10:11]
	s_mov_b32 m0, s46
	s_nop 0
	global_load_lds_dwordx4 v[146:147], off
	s_waitcnt vmcnt(8)
	s_waitcnt lgkmcnt(0)
	s_setprio 1
	s_barrier
	v_mfma_f32_16x16x32_bf16 v[62:65], v[154:157], v[186:189], v[62:65]
	v_mfma_f32_16x16x32_bf16 v[58:61], v[162:165], v[186:189], v[58:61]
	v_mfma_f32_16x16x32_bf16 v[54:57], v[154:157], v[194:197], v[54:57]
	v_mfma_f32_16x16x32_bf16 v[46:49], v[162:165], v[194:197], v[46:49]
	v_mfma_f32_16x16x32_bf16 v[38:41], v[154:157], v[202:205], v[38:41]
	v_mfma_f32_16x16x32_bf16 v[30:33], v[162:165], v[202:205], v[30:33]
	v_mfma_f32_16x16x32_bf16 v[22:25], v[154:157], v[210:213], v[22:25]
	v_mfma_f32_16x16x32_bf16 v[14:17], v[162:165], v[210:213], v[14:17]
	v_mfma_f32_16x16x32_bf16 v[62:65], v[158:161], v[190:193], v[62:65]
	v_mfma_f32_16x16x32_bf16 v[58:61], v[166:169], v[190:193], v[58:61]
	v_mfma_f32_16x16x32_bf16 v[54:57], v[158:161], v[198:201], v[54:57]
	v_mfma_f32_16x16x32_bf16 v[46:49], v[166:169], v[198:201], v[46:49]
	v_mfma_f32_16x16x32_bf16 v[38:41], v[158:161], v[206:209], v[38:41]
	v_mfma_f32_16x16x32_bf16 v[30:33], v[166:169], v[206:209], v[30:33]
	v_mfma_f32_16x16x32_bf16 v[22:25], v[158:161], v[214:217], v[22:25]
	v_mfma_f32_16x16x32_bf16 v[14:17], v[166:169], v[214:217], v[14:17]
	s_setprio 0
	s_setprio 1
	v_mfma_f32_16x16x32_bf16 v[50:53], v[170:173], v[186:189], v[50:53]
	v_mfma_f32_16x16x32_bf16 v[42:45], v[178:181], v[186:189], v[42:45]
	v_mfma_f32_16x16x32_bf16 v[34:37], v[170:173], v[194:197], v[34:37]
	v_mfma_f32_16x16x32_bf16 v[26:29], v[178:181], v[194:197], v[26:29]
	v_mfma_f32_16x16x32_bf16 v[18:21], v[170:173], v[202:205], v[18:21]
	v_mfma_f32_16x16x32_bf16 v[10:13], v[178:181], v[202:205], v[10:13]
	v_mfma_f32_16x16x32_bf16 v[6:9], v[170:173], v[210:213], v[6:9]
	v_mfma_f32_16x16x32_bf16 v[2:5], v[178:181], v[210:213], v[2:5]
	v_mfma_f32_16x16x32_bf16 v[50:53], v[174:177], v[190:193], v[50:53]
	v_mfma_f32_16x16x32_bf16 v[42:45], v[182:185], v[190:193], v[42:45]
	v_mfma_f32_16x16x32_bf16 v[34:37], v[174:177], v[198:201], v[34:37]
	v_mfma_f32_16x16x32_bf16 v[26:29], v[182:185], v[198:201], v[26:29]
	v_mfma_f32_16x16x32_bf16 v[18:21], v[174:177], v[206:209], v[18:21]
	v_mfma_f32_16x16x32_bf16 v[10:13], v[182:185], v[206:209], v[10:13]
	v_mfma_f32_16x16x32_bf16 v[6:9], v[174:177], v[214:217], v[6:9]
	v_mfma_f32_16x16x32_bf16 v[2:5], v[182:185], v[214:217], v[2:5]
	s_barrier
	s_setprio 0
	s_add_i32 s59, s59, 2
	s_add_u32 s30, s30, 0x100
	s_addc_u32 s31, s31, 0
	s_add_u32 s57, s57, 0x100
	s_addc_u32 s58, s58, 0
	s_cmp_gt_u32 s59, 29
	.p2alignl 6, 3212836864

.LBB0_1478:
	s_ashr_i32 s19, s18, 31
	s_lshl_b64 s[22:23], s[18:19], 20
	s_add_u32 s22, s20, s22
	s_addc_u32 s23, s21, s23
	s_and_b64 s[24:25], s[8:9], exec
	s_cselect_b32 s19, s23, s29
	s_cselect_b32 s27, s22, s28
	s_ashr_i32 s17, s16, 31
	s_lshl_b64 s[24:25], s[16:17], 20
	s_add_u32 s24, s15, s24
	s_addc_u32 s25, s33, s25
	s_and_b64 s[34:35], s[8:9], exec
	s_cselect_b32 s17, s25, s31
	s_cselect_b32 s51, s24, s30
	s_lshl_b32 s34, s26, 8
	s_ashr_i32 s35, s34, 31
	v_lshl_add_u64 v[238:239], s[34:35], 2, v[138:139]
	global_load_dword v240, v[238:239], off
	global_load_dword v242, v[238:239], off offset:64
	global_load_dword v244, v[238:239], off offset:128
	global_load_dword v246, v[238:239], off offset:192
	global_load_dword v248, v[238:239], off offset:512
	global_load_dword v250, v[238:239], off offset:576
	global_load_dword v252, v[238:239], off offset:640
	global_load_dword v238, v[238:239], off offset:704
	s_add_u32 s28, s28, 0x80080
	s_addc_u32 s29, s29, 0
	s_add_u32 s52, s30, 0x100
	s_addc_u32 s53, s31, 0
	s_mov_b32 s54, -2
	s_waitcnt vmcnt(0)
	ds_read_b128 v[154:157], v150
	ds_read_b128 v[158:161], v150 offset:1024
	ds_read_b128 v[162:165], v150 offset:2048
	ds_read_b128 v[166:169], v150 offset:3072
	ds_read_b128 v[170:173], v151
	ds_read_b128 v[174:177], v151 offset:1024
	ds_read_b128 v[178:181], v151 offset:2048
	ds_read_b128 v[182:185], v151 offset:3072
	s_add_u32 s30, s28, 0xfff80080
	s_addc_u32 s31, s29, -1
	s_cmp_eq_u32 s54, 28
	s_cselect_b32 s35, s19, s31
	s_cselect_b32 s34, s27, s30
	s_cselect_b32 s31, s17, s53
	s_cselect_b32 s30, s51, s52
	v_lshl_add_u64 v[218:219], s[28:29], 0, v[140:141]
	s_add_i32 m0, s39, 0xc000
	ds_read_b128 v[186:189], v152
	ds_read_b128 v[190:193], v152 offset:1024
	ds_read_b128 v[194:197], v152 offset:2048
	ds_read_b128 v[198:201], v152 offset:3072
	ds_read_b128 v[202:205], v152 offset:4096
	ds_read_b128 v[206:209], v152 offset:5120
	ds_read_b128 v[210:213], v152 offset:6144
	ds_read_b128 v[214:217], v152 offset:7168
	global_load_lds_dwordx4 v[218:219], off
	v_lshl_add_u64 v[218:219], s[28:29], 0, v[142:143]
	s_add_i32 m0, s39, 0xe000
	s_nop 0
	global_load_lds_dwordx4 v[218:219], off
	s_waitcnt vmcnt(8)
	s_waitcnt lgkmcnt(0)
	s_setprio 1
	s_barrier
	v_mfma_f32_16x16x32_bf16 v[126:129], v[154:157], v[186:189], 0
	v_mfma_f32_16x16x32_bf16 v[122:125], v[162:165], v[186:189], 0
	v_mfma_f32_16x16x32_bf16 v[118:121], v[154:157], v[194:197], 0
	v_mfma_f32_16x16x32_bf16 v[114:117], v[162:165], v[194:197], 0
	v_mfma_f32_16x16x32_bf16 v[110:113], v[154:157], v[202:205], 0
	v_mfma_f32_16x16x32_bf16 v[102:105], v[162:165], v[202:205], 0
	v_mfma_f32_16x16x32_bf16 v[94:97], v[154:157], v[210:213], 0
	v_mfma_f32_16x16x32_bf16 v[86:89], v[162:165], v[210:213], 0
	v_mfma_f32_16x16x32_bf16 v[126:129], v[158:161], v[190:193], v[126:129]
	v_mfma_f32_16x16x32_bf16 v[122:125], v[166:169], v[190:193], v[122:125]
	v_mfma_f32_16x16x32_bf16 v[118:121], v[158:161], v[198:201], v[118:121]
	v_mfma_f32_16x16x32_bf16 v[114:117], v[166:169], v[198:201], v[114:117]
	v_mfma_f32_16x16x32_bf16 v[110:113], v[158:161], v[206:209], v[110:113]
	v_mfma_f32_16x16x32_bf16 v[102:105], v[166:169], v[206:209], v[102:105]
	v_mfma_f32_16x16x32_bf16 v[94:97], v[158:161], v[214:217], v[94:97]
	v_mfma_f32_16x16x32_bf16 v[86:89], v[166:169], v[214:217], v[86:89]
	s_setprio 0
	s_setprio 1
	v_mfma_f32_16x16x32_bf16 v[106:109], v[170:173], v[186:189], 0
	v_mfma_f32_16x16x32_bf16 v[98:101], v[178:181], v[186:189], 0
	v_mfma_f32_16x16x32_bf16 v[90:93], v[170:173], v[194:197], 0
	v_mfma_f32_16x16x32_bf16 v[82:85], v[178:181], v[194:197], 0
	v_mfma_f32_16x16x32_bf16 v[78:81], v[170:173], v[202:205], 0
	v_mfma_f32_16x16x32_bf16 v[74:77], v[178:181], v[202:205], 0
	v_mfma_f32_16x16x32_bf16 v[70:73], v[170:173], v[210:213], 0
	v_mfma_f32_16x16x32_bf16 v[66:69], v[178:181], v[210:213], 0
	v_mfma_f32_16x16x32_bf16 v[106:109], v[174:177], v[190:193], v[106:109]
	v_mfma_f32_16x16x32_bf16 v[98:101], v[182:185], v[190:193], v[98:101]
	v_mfma_f32_16x16x32_bf16 v[90:93], v[174:177], v[198:201], v[90:93]
	v_mfma_f32_16x16x32_bf16 v[82:85], v[182:185], v[198:201], v[82:85]
	v_mfma_f32_16x16x32_bf16 v[78:81], v[174:177], v[206:209], v[78:81]
	v_mfma_f32_16x16x32_bf16 v[74:77], v[182:185], v[206:209], v[74:77]
	v_mfma_f32_16x16x32_bf16 v[70:73], v[174:177], v[214:217], v[70:73]
	v_mfma_f32_16x16x32_bf16 v[66:69], v[182:185], v[214:217], v[66:69]
	s_barrier
	s_setprio 0
	s_add_i32 s55, s47, s36
	v_lshl_add_u64 v[218:219], s[30:31], 0, v[134:135]
	s_mov_b32 m0, s55
	ds_read_b128 v[186:189], v152 offset:16384
	ds_read_b128 v[190:193], v152 offset:17408
	ds_read_b128 v[194:197], v152 offset:18432
	ds_read_b128 v[198:201], v152 offset:19456
	ds_read_b128 v[202:205], v152 offset:20480
	ds_read_b128 v[206:209], v152 offset:21504
	ds_read_b128 v[210:213], v152 offset:22528
	ds_read_b128 v[214:217], v152 offset:23552
	global_load_lds_dwordx4 v[218:219], off
	s_add_i32 m0, s55, 0x2000
	s_add_u32 s56, s30, 0x80000
	v_lshl_add_u64 v[220:221], s[30:31], 0, v[130:131]
	s_addc_u32 s57, s31, 0
	s_add_i32 s55, s48, s36
	global_load_lds_dwordx4 v[220:221], off
	v_lshl_add_u64 v[222:223], s[56:57], 0, v[134:135]
	s_mov_b32 m0, s55
	v_lshl_add_u64 v[224:225], s[34:35], 0, v[132:133]
	global_load_lds_dwordx4 v[222:223], off
	v_lshl_add_u64 v[222:223], s[56:57], 0, v[130:131]
	s_add_i32 m0, s55, 0x2000
	s_nop 0
	global_load_lds_dwordx4 v[222:223], off
	v_lshl_add_u64 v[222:223], s[34:35], 0, v[136:137]
	s_mov_b32 m0, s39
	s_nop 0
	global_load_lds_dwordx4 v[222:223], off
	s_mov_b32 m0, s40
	s_nop 0
	global_load_lds_dwordx4 v[224:225], off
	s_waitcnt vmcnt(8)
	s_waitcnt lgkmcnt(0)
	s_setprio 1
	s_barrier
	v_mfma_f32_16x16x32_bf16 v[62:65], v[154:157], v[186:189], 0
	v_mfma_f32_16x16x32_bf16 v[58:61], v[162:165], v[186:189], 0
	v_mfma_f32_16x16x32_bf16 v[54:57], v[154:157], v[194:197], 0
	v_mfma_f32_16x16x32_bf16 v[50:53], v[162:165], v[194:197], 0
	v_mfma_f32_16x16x32_bf16 v[46:49], v[154:157], v[202:205], 0
	v_mfma_f32_16x16x32_bf16 v[38:41], v[162:165], v[202:205], 0
	v_mfma_f32_16x16x32_bf16 v[30:33], v[154:157], v[210:213], 0
	v_mfma_f32_16x16x32_bf16 v[22:25], v[162:165], v[210:213], 0
	v_mfma_f32_16x16x32_bf16 v[62:65], v[158:161], v[190:193], v[62:65]
	v_mfma_f32_16x16x32_bf16 v[58:61], v[166:169], v[190:193], v[58:61]
	v_mfma_f32_16x16x32_bf16 v[54:57], v[158:161], v[198:201], v[54:57]
	v_mfma_f32_16x16x32_bf16 v[50:53], v[166:169], v[198:201], v[50:53]
	v_mfma_f32_16x16x32_bf16 v[46:49], v[158:161], v[206:209], v[46:49]
	v_mfma_f32_16x16x32_bf16 v[38:41], v[166:169], v[206:209], v[38:41]
	v_mfma_f32_16x16x32_bf16 v[30:33], v[158:161], v[214:217], v[30:33]
	v_mfma_f32_16x16x32_bf16 v[22:25], v[166:169], v[214:217], v[22:25]
	s_setprio 0
	s_setprio 1
	v_mfma_f32_16x16x32_bf16 v[42:45], v[170:173], v[186:189], 0
	v_mfma_f32_16x16x32_bf16 v[34:37], v[178:181], v[186:189], 0
	v_mfma_f32_16x16x32_bf16 v[26:29], v[170:173], v[194:197], 0
	v_mfma_f32_16x16x32_bf16 v[18:21], v[178:181], v[194:197], 0
	v_mfma_f32_16x16x32_bf16 v[14:17], v[170:173], v[202:205], 0
	v_mfma_f32_16x16x32_bf16 v[10:13], v[178:181], v[202:205], 0
	v_mfma_f32_16x16x32_bf16 v[6:9], v[170:173], v[210:213], 0
	v_mfma_f32_16x16x32_bf16 v[2:5], v[178:181], v[210:213], 0
	v_mfma_f32_16x16x32_bf16 v[42:45], v[174:177], v[190:193], v[42:45]
	v_mfma_f32_16x16x32_bf16 v[34:37], v[182:185], v[190:193], v[34:37]
	v_mfma_f32_16x16x32_bf16 v[26:29], v[174:177], v[198:201], v[26:29]
	v_mfma_f32_16x16x32_bf16 v[18:21], v[182:185], v[198:201], v[18:21]
	v_mfma_f32_16x16x32_bf16 v[14:17], v[174:177], v[206:209], v[14:17]
	v_mfma_f32_16x16x32_bf16 v[10:13], v[182:185], v[206:209], v[10:13]
	v_mfma_f32_16x16x32_bf16 v[6:9], v[174:177], v[214:217], v[6:9]
	v_mfma_f32_16x16x32_bf16 v[2:5], v[182:185], v[214:217], v[2:5]
	s_barrier
	s_setprio 0
	s_add_i32 s55, 0, 0x18000
	v_add_u32_e32 v153, s55, v148
	s_add_i32 s56, 0, 0x1c000
	ds_read_b128 v[154:157], v153
	ds_read_b128 v[158:161], v153 offset:1024
	ds_read_b128 v[162:165], v153 offset:2048
	ds_read_b128 v[166:169], v153 offset:3072
	v_add_u32_e32 v153, s56, v148
	ds_read_b128 v[170:173], v153
	ds_read_b128 v[174:177], v153 offset:1024
	ds_read_b128 v[178:181], v153 offset:2048
	ds_read_b128 v[182:185], v153 offset:3072
	s_add_u32 s34, s34, 0x80000
	s_addc_u32 s35, s35, 0
	s_mov_b32 m0, s41
	v_lshl_add_u64 v[226:227], s[34:35], 0, v[136:137]
	ds_read_b128 v[186:189], v152 offset:32768
	ds_read_b128 v[190:193], v152 offset:33792
	ds_read_b128 v[194:197], v152 offset:34816
	ds_read_b128 v[198:201], v152 offset:35840
	ds_read_b128 v[202:205], v152 offset:36864
	ds_read_b128 v[206:209], v152 offset:37888
	ds_read_b128 v[210:213], v152 offset:38912
	ds_read_b128 v[214:217], v152 offset:39936
	global_load_lds_dwordx4 v[226:227], off
	v_lshl_add_u64 v[226:227], s[34:35], 0, v[132:133]
	s_mov_b32 m0, s42
	s_nop 0
	global_load_lds_dwordx4 v[226:227], off
	s_waitcnt vmcnt(8)
	s_waitcnt lgkmcnt(0)
	s_setprio 1
	s_barrier
	v_mfma_f32_16x16x32_bf16 v[126:129], v[154:157], v[186:189], v[126:129]
	v_mfma_f32_16x16x32_bf16 v[122:125], v[162:165], v[186:189], v[122:125]
	v_mfma_f32_16x16x32_bf16 v[118:121], v[154:157], v[194:197], v[118:121]
	v_mfma_f32_16x16x32_bf16 v[114:117], v[162:165], v[194:197], v[114:117]
	v_mfma_f32_16x16x32_bf16 v[110:113], v[154:157], v[202:205], v[110:113]
	v_mfma_f32_16x16x32_bf16 v[102:105], v[162:165], v[202:205], v[102:105]
	v_mfma_f32_16x16x32_bf16 v[94:97], v[154:157], v[210:213], v[94:97]
	v_mfma_f32_16x16x32_bf16 v[86:89], v[162:165], v[210:213], v[86:89]
	v_mfma_f32_16x16x32_bf16 v[126:129], v[158:161], v[190:193], v[126:129]
	v_mfma_f32_16x16x32_bf16 v[122:125], v[166:169], v[190:193], v[122:125]
	v_mfma_f32_16x16x32_bf16 v[118:121], v[158:161], v[198:201], v[118:121]
	v_mfma_f32_16x16x32_bf16 v[114:117], v[166:169], v[198:201], v[114:117]
	v_mfma_f32_16x16x32_bf16 v[110:113], v[158:161], v[206:209], v[110:113]
	v_mfma_f32_16x16x32_bf16 v[102:105], v[166:169], v[206:209], v[102:105]
	v_mfma_f32_16x16x32_bf16 v[94:97], v[158:161], v[214:217], v[94:97]
	v_mfma_f32_16x16x32_bf16 v[86:89], v[166:169], v[214:217], v[86:89]
	s_setprio 0
	s_setprio 1
	v_mfma_f32_16x16x32_bf16 v[106:109], v[170:173], v[186:189], v[106:109]
	v_mfma_f32_16x16x32_bf16 v[98:101], v[178:181], v[186:189], v[98:101]
	v_mfma_f32_16x16x32_bf16 v[90:93], v[170:173], v[194:197], v[90:93]
	v_mfma_f32_16x16x32_bf16 v[82:85], v[178:181], v[194:197], v[82:85]
	v_mfma_f32_16x16x32_bf16 v[78:81], v[170:173], v[202:205], v[78:81]
	v_mfma_f32_16x16x32_bf16 v[74:77], v[178:181], v[202:205], v[74:77]
	v_mfma_f32_16x16x32_bf16 v[70:73], v[170:173], v[210:213], v[70:73]
	v_mfma_f32_16x16x32_bf16 v[66:69], v[178:181], v[210:213], v[66:69]
	v_mfma_f32_16x16x32_bf16 v[106:109], v[174:177], v[190:193], v[106:109]
	v_mfma_f32_16x16x32_bf16 v[98:101], v[182:185], v[190:193], v[98:101]
	v_mfma_f32_16x16x32_bf16 v[90:93], v[174:177], v[198:201], v[90:93]
	v_mfma_f32_16x16x32_bf16 v[82:85], v[182:185], v[198:201], v[82:85]
	v_mfma_f32_16x16x32_bf16 v[78:81], v[174:177], v[206:209], v[78:81]
	v_mfma_f32_16x16x32_bf16 v[74:77], v[182:185], v[206:209], v[74:77]
	v_mfma_f32_16x16x32_bf16 v[70:73], v[174:177], v[214:217], v[70:73]
	v_mfma_f32_16x16x32_bf16 v[66:69], v[182:185], v[214:217], v[66:69]
	s_barrier
	s_setprio 0
	s_add_i32 s34, s55, s36
	v_lshl_add_u64 v[218:219], v[218:219], 0, s[10:11]
	s_mov_b32 m0, s34
	ds_read_b128 v[186:189], v152 offset:49152
	ds_read_b128 v[190:193], v152 offset:50176
	ds_read_b128 v[194:197], v152 offset:51200
	ds_read_b128 v[198:201], v152 offset:52224
	ds_read_b128 v[202:205], v152 offset:53248
	ds_read_b128 v[206:209], v152 offset:54272
	ds_read_b128 v[210:213], v152 offset:55296
	ds_read_b128 v[214:217], v152 offset:56320
	global_load_lds_dwordx4 v[218:219], off
	s_add_i32 m0, s34, 0x2000
	s_add_u32 s30, s30, 0x80080
	v_lshl_add_u64 v[218:219], v[220:221], 0, s[10:11]
	s_addc_u32 s31, s31, 0
	s_add_i32 s34, s56, s36
	global_load_lds_dwordx4 v[218:219], off
	v_lshl_add_u64 v[218:219], s[30:31], 0, v[134:135]
	s_mov_b32 m0, s34
	s_nop 0
	global_load_lds_dwordx4 v[218:219], off
	v_lshl_add_u64 v[218:219], s[30:31], 0, v[130:131]
	s_add_i32 m0, s34, 0x2000
	s_nop 0
	global_load_lds_dwordx4 v[218:219], off
	v_lshl_add_u64 v[218:219], v[222:223], 0, s[10:11]
	s_mov_b32 m0, s44
	s_nop 0
	global_load_lds_dwordx4 v[218:219], off
	v_lshl_add_u64 v[218:219], v[224:225], 0, s[10:11]
	s_mov_b32 m0, s45
	s_nop 0
	global_load_lds_dwordx4 v[218:219], off
	s_waitcnt vmcnt(8)
	s_waitcnt lgkmcnt(0)
	s_setprio 1
	s_barrier
	v_mfma_f32_16x16x32_bf16 v[62:65], v[154:157], v[186:189], v[62:65]
	v_mfma_f32_16x16x32_bf16 v[58:61], v[162:165], v[186:189], v[58:61]
	v_mfma_f32_16x16x32_bf16 v[54:57], v[154:157], v[194:197], v[54:57]
	v_mfma_f32_16x16x32_bf16 v[50:53], v[162:165], v[194:197], v[50:53]
	v_mfma_f32_16x16x32_bf16 v[46:49], v[154:157], v[202:205], v[46:49]
	v_mfma_f32_16x16x32_bf16 v[38:41], v[162:165], v[202:205], v[38:41]
	v_mfma_f32_16x16x32_bf16 v[30:33], v[154:157], v[210:213], v[30:33]
	v_mfma_f32_16x16x32_bf16 v[22:25], v[162:165], v[210:213], v[22:25]
	v_mfma_f32_16x16x32_bf16 v[62:65], v[158:161], v[190:193], v[62:65]
	v_mfma_f32_16x16x32_bf16 v[58:61], v[166:169], v[190:193], v[58:61]
	v_mfma_f32_16x16x32_bf16 v[54:57], v[158:161], v[198:201], v[54:57]
	v_mfma_f32_16x16x32_bf16 v[50:53], v[166:169], v[198:201], v[50:53]
	v_mfma_f32_16x16x32_bf16 v[46:49], v[158:161], v[206:209], v[46:49]
	v_mfma_f32_16x16x32_bf16 v[38:41], v[166:169], v[206:209], v[38:41]
	v_mfma_f32_16x16x32_bf16 v[30:33], v[158:161], v[214:217], v[30:33]
	v_mfma_f32_16x16x32_bf16 v[22:25], v[166:169], v[214:217], v[22:25]
	s_setprio 0
	s_setprio 1
	v_mfma_f32_16x16x32_bf16 v[42:45], v[170:173], v[186:189], v[42:45]
	v_mfma_f32_16x16x32_bf16 v[34:37], v[178:181], v[186:189], v[34:37]
	v_mfma_f32_16x16x32_bf16 v[26:29], v[170:173], v[194:197], v[26:29]
	v_mfma_f32_16x16x32_bf16 v[18:21], v[178:181], v[194:197], v[18:21]
	v_mfma_f32_16x16x32_bf16 v[14:17], v[170:173], v[202:205], v[14:17]
	v_mfma_f32_16x16x32_bf16 v[10:13], v[178:181], v[202:205], v[10:13]
	v_mfma_f32_16x16x32_bf16 v[6:9], v[170:173], v[210:213], v[6:9]
	v_mfma_f32_16x16x32_bf16 v[2:5], v[178:181], v[210:213], v[2:5]
	v_mfma_f32_16x16x32_bf16 v[42:45], v[174:177], v[190:193], v[42:45]
	v_mfma_f32_16x16x32_bf16 v[34:37], v[182:185], v[190:193], v[34:37]
	v_mfma_f32_16x16x32_bf16 v[26:29], v[174:177], v[198:201], v[26:29]
	v_mfma_f32_16x16x32_bf16 v[18:21], v[182:185], v[198:201], v[18:21]
	v_mfma_f32_16x16x32_bf16 v[14:17], v[174:177], v[206:209], v[14:17]
	v_mfma_f32_16x16x32_bf16 v[10:13], v[182:185], v[206:209], v[10:13]
	v_mfma_f32_16x16x32_bf16 v[6:9], v[174:177], v[214:217], v[6:9]
	v_mfma_f32_16x16x32_bf16 v[2:5], v[182:185], v[214:217], v[2:5]
	s_barrier
	s_setprio 0
	s_add_i32 s54, s54, 2
	s_add_u32 s28, s28, 0x100
	s_addc_u32 s29, s29, 0
	s_add_u32 s52, s52, 0x100
	s_addc_u32 s53, s53, 0
	s_cmp_gt_u32 s54, 29
	.p2alignl 6, 3212836864

.LBB0_1561:
	s_add_u32 s26, s26, 0x160080
	s_addc_u32 s27, s27, 0
	s_add_u32 s57, s28, 0x100
	s_addc_u32 s58, s29, 0
	s_mov_b32 s59, -2
	ds_read_b128 v[154:157], v150
	ds_read_b128 v[158:161], v150 offset:1024
	ds_read_b128 v[162:165], v150 offset:2048
	ds_read_b128 v[166:169], v150 offset:3072
	ds_read_b128 v[170:173], v151
	ds_read_b128 v[174:177], v151 offset:1024
	ds_read_b128 v[178:181], v151 offset:2048
	ds_read_b128 v[182:185], v151 offset:3072
	s_add_u32 s28, s26, 0xffea0080
	s_addc_u32 s29, s27, -1
	s_cmpk_eq_i32 s59, 0x54
	s_cselect_b32 s31, s1, s29
	s_cselect_b32 s30, s0, s28
	s_cselect_b32 s29, s25, s58
	s_cselect_b32 s28, s24, s57
	v_lshl_add_u64 v[146:147], s[26:27], 0, v[138:139]
	s_add_i32 m0, s39, 0xc000
	ds_read_b128 v[186:189], v152
	ds_read_b128 v[190:193], v152 offset:1024
	ds_read_b128 v[194:197], v152 offset:2048
	ds_read_b128 v[198:201], v152 offset:3072
	ds_read_b128 v[202:205], v152 offset:4096
	ds_read_b128 v[206:209], v152 offset:5120
	ds_read_b128 v[210:213], v152 offset:6144
	ds_read_b128 v[214:217], v152 offset:7168
	global_load_lds_dwordx4 v[146:147], off
	v_lshl_add_u64 v[146:147], s[26:27], 0, v[140:141]
	s_add_i32 m0, s39, 0xe000
	s_nop 0
	global_load_lds_dwordx4 v[146:147], off
	s_waitcnt vmcnt(8)
	s_waitcnt lgkmcnt(0)
	s_setprio 1
	s_barrier
	v_mfma_f32_16x16x32_bf16 v[126:129], v[154:157], v[186:189], 0
	v_mfma_f32_16x16x32_bf16 v[122:125], v[162:165], v[186:189], 0
	v_mfma_f32_16x16x32_bf16 v[118:121], v[154:157], v[194:197], 0
	v_mfma_f32_16x16x32_bf16 v[110:113], v[162:165], v[194:197], 0
	v_mfma_f32_16x16x32_bf16 v[102:105], v[154:157], v[202:205], 0
	v_mfma_f32_16x16x32_bf16 v[94:97], v[162:165], v[202:205], 0
	v_mfma_f32_16x16x32_bf16 v[86:89], v[154:157], v[210:213], 0
	v_mfma_f32_16x16x32_bf16 v[78:81], v[162:165], v[210:213], 0
	v_mfma_f32_16x16x32_bf16 v[126:129], v[158:161], v[190:193], v[126:129]
	v_mfma_f32_16x16x32_bf16 v[122:125], v[166:169], v[190:193], v[122:125]
	v_mfma_f32_16x16x32_bf16 v[118:121], v[158:161], v[198:201], v[118:121]
	v_mfma_f32_16x16x32_bf16 v[110:113], v[166:169], v[198:201], v[110:113]
	v_mfma_f32_16x16x32_bf16 v[102:105], v[158:161], v[206:209], v[102:105]
	v_mfma_f32_16x16x32_bf16 v[94:97], v[166:169], v[206:209], v[94:97]
	v_mfma_f32_16x16x32_bf16 v[86:89], v[158:161], v[214:217], v[86:89]
	v_mfma_f32_16x16x32_bf16 v[78:81], v[166:169], v[214:217], v[78:81]
	s_setprio 0
	s_setprio 1
	v_mfma_f32_16x16x32_bf16 v[114:117], v[170:173], v[186:189], 0
	v_mfma_f32_16x16x32_bf16 v[106:109], v[178:181], v[186:189], 0
	v_mfma_f32_16x16x32_bf16 v[98:101], v[170:173], v[194:197], 0
	v_mfma_f32_16x16x32_bf16 v[90:93], v[178:181], v[194:197], 0
	v_mfma_f32_16x16x32_bf16 v[82:85], v[170:173], v[202:205], 0
	v_mfma_f32_16x16x32_bf16 v[74:77], v[178:181], v[202:205], 0
	v_mfma_f32_16x16x32_bf16 v[70:73], v[170:173], v[210:213], 0
	v_mfma_f32_16x16x32_bf16 v[66:69], v[178:181], v[210:213], 0
	v_mfma_f32_16x16x32_bf16 v[114:117], v[174:177], v[190:193], v[114:117]
	v_mfma_f32_16x16x32_bf16 v[106:109], v[182:185], v[190:193], v[106:109]
	v_mfma_f32_16x16x32_bf16 v[98:101], v[174:177], v[198:201], v[98:101]
	v_mfma_f32_16x16x32_bf16 v[90:93], v[182:185], v[198:201], v[90:93]
	v_mfma_f32_16x16x32_bf16 v[82:85], v[174:177], v[206:209], v[82:85]
	v_mfma_f32_16x16x32_bf16 v[74:77], v[182:185], v[206:209], v[74:77]
	v_mfma_f32_16x16x32_bf16 v[70:73], v[174:177], v[214:217], v[70:73]
	v_mfma_f32_16x16x32_bf16 v[66:69], v[182:185], v[214:217], v[66:69]
	s_barrier
	s_setprio 0
	s_add_i32 s60, s47, s38
	v_lshl_add_u64 v[146:147], s[28:29], 0, v[132:133]
	s_mov_b32 m0, s60
	ds_read_b128 v[186:189], v152 offset:16384
	ds_read_b128 v[190:193], v152 offset:17408
	ds_read_b128 v[194:197], v152 offset:18432
	ds_read_b128 v[198:201], v152 offset:19456
	ds_read_b128 v[202:205], v152 offset:20480
	ds_read_b128 v[206:209], v152 offset:21504
	ds_read_b128 v[210:213], v152 offset:22528
	ds_read_b128 v[214:217], v152 offset:23552
	global_load_lds_dwordx4 v[146:147], off
	s_add_i32 m0, s60, 0x2000
	s_add_u32 s60, s28, 0x160000
	v_lshl_add_u64 v[218:219], s[28:29], 0, v[136:137]
	s_addc_u32 s61, s29, 0
	s_add_i32 s62, s48, s38
	global_load_lds_dwordx4 v[218:219], off
	v_lshl_add_u64 v[220:221], s[60:61], 0, v[132:133]
	s_mov_b32 m0, s62
	v_lshl_add_u64 v[222:223], s[30:31], 0, v[134:135]
	global_load_lds_dwordx4 v[220:221], off
	v_lshl_add_u64 v[220:221], s[60:61], 0, v[136:137]
	s_add_i32 m0, s62, 0x2000
	s_nop 0
	global_load_lds_dwordx4 v[220:221], off
	v_lshl_add_u64 v[220:221], s[30:31], 0, v[130:131]
	s_mov_b32 m0, s39
	s_nop 0
	global_load_lds_dwordx4 v[220:221], off
	s_mov_b32 m0, s40
	s_nop 0
	global_load_lds_dwordx4 v[222:223], off
	s_waitcnt vmcnt(8)
	s_waitcnt lgkmcnt(0)
	s_setprio 1
	s_barrier
	v_mfma_f32_16x16x32_bf16 v[62:65], v[154:157], v[186:189], 0
	v_mfma_f32_16x16x32_bf16 v[58:61], v[162:165], v[186:189], 0
	v_mfma_f32_16x16x32_bf16 v[54:57], v[154:157], v[194:197], 0
	v_mfma_f32_16x16x32_bf16 v[46:49], v[162:165], v[194:197], 0
	v_mfma_f32_16x16x32_bf16 v[38:41], v[154:157], v[202:205], 0
	v_mfma_f32_16x16x32_bf16 v[30:33], v[162:165], v[202:205], 0
	v_mfma_f32_16x16x32_bf16 v[22:25], v[154:157], v[210:213], 0
	v_mfma_f32_16x16x32_bf16 v[14:17], v[162:165], v[210:213], 0
	v_mfma_f32_16x16x32_bf16 v[62:65], v[158:161], v[190:193], v[62:65]
	v_mfma_f32_16x16x32_bf16 v[58:61], v[166:169], v[190:193], v[58:61]
	v_mfma_f32_16x16x32_bf16 v[54:57], v[158:161], v[198:201], v[54:57]
	v_mfma_f32_16x16x32_bf16 v[46:49], v[166:169], v[198:201], v[46:49]
	v_mfma_f32_16x16x32_bf16 v[38:41], v[158:161], v[206:209], v[38:41]
	v_mfma_f32_16x16x32_bf16 v[30:33], v[166:169], v[206:209], v[30:33]
	v_mfma_f32_16x16x32_bf16 v[22:25], v[158:161], v[214:217], v[22:25]
	v_mfma_f32_16x16x32_bf16 v[14:17], v[166:169], v[214:217], v[14:17]
	s_setprio 0
	s_setprio 1
	v_mfma_f32_16x16x32_bf16 v[50:53], v[170:173], v[186:189], 0
	v_mfma_f32_16x16x32_bf16 v[42:45], v[178:181], v[186:189], 0
	v_mfma_f32_16x16x32_bf16 v[34:37], v[170:173], v[194:197], 0
	v_mfma_f32_16x16x32_bf16 v[26:29], v[178:181], v[194:197], 0
	v_mfma_f32_16x16x32_bf16 v[18:21], v[170:173], v[202:205], 0
	v_mfma_f32_16x16x32_bf16 v[10:13], v[178:181], v[202:205], 0
	v_mfma_f32_16x16x32_bf16 v[6:9], v[170:173], v[210:213], 0
	v_mfma_f32_16x16x32_bf16 v[2:5], v[178:181], v[210:213], 0
	v_mfma_f32_16x16x32_bf16 v[50:53], v[174:177], v[190:193], v[50:53]
	v_mfma_f32_16x16x32_bf16 v[42:45], v[182:185], v[190:193], v[42:45]
	v_mfma_f32_16x16x32_bf16 v[34:37], v[174:177], v[198:201], v[34:37]
	v_mfma_f32_16x16x32_bf16 v[26:29], v[182:185], v[198:201], v[26:29]
	v_mfma_f32_16x16x32_bf16 v[18:21], v[174:177], v[206:209], v[18:21]
	v_mfma_f32_16x16x32_bf16 v[10:13], v[182:185], v[206:209], v[10:13]
	v_mfma_f32_16x16x32_bf16 v[6:9], v[174:177], v[214:217], v[6:9]
	v_mfma_f32_16x16x32_bf16 v[2:5], v[182:185], v[214:217], v[2:5]
	s_barrier
	s_setprio 0
	s_add_i32 s60, 0, 0x18000
	v_add_u32_e32 v153, s60, v148
	s_add_i32 s61, 0, 0x1c000
	ds_read_b128 v[154:157], v153
	ds_read_b128 v[158:161], v153 offset:1024
	ds_read_b128 v[162:165], v153 offset:2048
	ds_read_b128 v[166:169], v153 offset:3072
	v_add_u32_e32 v153, s61, v148
	ds_read_b128 v[170:173], v153
	ds_read_b128 v[174:177], v153 offset:1024
	ds_read_b128 v[178:181], v153 offset:2048
	ds_read_b128 v[182:185], v153 offset:3072
	s_add_u32 s30, s30, 0x160000
	s_addc_u32 s31, s31, 0
	s_mov_b32 m0, s41
	v_lshl_add_u64 v[224:225], s[30:31], 0, v[130:131]
	ds_read_b128 v[186:189], v152 offset:32768
	ds_read_b128 v[190:193], v152 offset:33792
	ds_read_b128 v[194:197], v152 offset:34816
	ds_read_b128 v[198:201], v152 offset:35840
	ds_read_b128 v[202:205], v152 offset:36864
	ds_read_b128 v[206:209], v152 offset:37888
	ds_read_b128 v[210:213], v152 offset:38912
	ds_read_b128 v[214:217], v152 offset:39936
	global_load_lds_dwordx4 v[224:225], off
	v_lshl_add_u64 v[224:225], s[30:31], 0, v[134:135]
	s_mov_b32 m0, s42
	s_nop 0
	global_load_lds_dwordx4 v[224:225], off
	s_waitcnt vmcnt(8)
	s_waitcnt lgkmcnt(0)
	s_setprio 1
	s_barrier
	v_mfma_f32_16x16x32_bf16 v[126:129], v[154:157], v[186:189], v[126:129]
	v_mfma_f32_16x16x32_bf16 v[122:125], v[162:165], v[186:189], v[122:125]
	v_mfma_f32_16x16x32_bf16 v[118:121], v[154:157], v[194:197], v[118:121]
	v_mfma_f32_16x16x32_bf16 v[110:113], v[162:165], v[194:197], v[110:113]
	v_mfma_f32_16x16x32_bf16 v[102:105], v[154:157], v[202:205], v[102:105]
	v_mfma_f32_16x16x32_bf16 v[94:97], v[162:165], v[202:205], v[94:97]
	v_mfma_f32_16x16x32_bf16 v[86:89], v[154:157], v[210:213], v[86:89]
	v_mfma_f32_16x16x32_bf16 v[78:81], v[162:165], v[210:213], v[78:81]
	v_mfma_f32_16x16x32_bf16 v[126:129], v[158:161], v[190:193], v[126:129]
	v_mfma_f32_16x16x32_bf16 v[122:125], v[166:169], v[190:193], v[122:125]
	v_mfma_f32_16x16x32_bf16 v[118:121], v[158:161], v[198:201], v[118:121]
	v_mfma_f32_16x16x32_bf16 v[110:113], v[166:169], v[198:201], v[110:113]
	v_mfma_f32_16x16x32_bf16 v[102:105], v[158:161], v[206:209], v[102:105]
	v_mfma_f32_16x16x32_bf16 v[94:97], v[166:169], v[206:209], v[94:97]
	v_mfma_f32_16x16x32_bf16 v[86:89], v[158:161], v[214:217], v[86:89]
	v_mfma_f32_16x16x32_bf16 v[78:81], v[166:169], v[214:217], v[78:81]
	s_setprio 0
	s_setprio 1
	v_mfma_f32_16x16x32_bf16 v[114:117], v[170:173], v[186:189], v[114:117]
	v_mfma_f32_16x16x32_bf16 v[106:109], v[178:181], v[186:189], v[106:109]
	v_mfma_f32_16x16x32_bf16 v[98:101], v[170:173], v[194:197], v[98:101]
	v_mfma_f32_16x16x32_bf16 v[90:93], v[178:181], v[194:197], v[90:93]
	v_mfma_f32_16x16x32_bf16 v[82:85], v[170:173], v[202:205], v[82:85]
	v_mfma_f32_16x16x32_bf16 v[74:77], v[178:181], v[202:205], v[74:77]
	v_mfma_f32_16x16x32_bf16 v[70:73], v[170:173], v[210:213], v[70:73]
	v_mfma_f32_16x16x32_bf16 v[66:69], v[178:181], v[210:213], v[66:69]
	v_mfma_f32_16x16x32_bf16 v[114:117], v[174:177], v[190:193], v[114:117]
	v_mfma_f32_16x16x32_bf16 v[106:109], v[182:185], v[190:193], v[106:109]
	v_mfma_f32_16x16x32_bf16 v[98:101], v[174:177], v[198:201], v[98:101]
	v_mfma_f32_16x16x32_bf16 v[90:93], v[182:185], v[198:201], v[90:93]
	v_mfma_f32_16x16x32_bf16 v[82:85], v[174:177], v[206:209], v[82:85]
	v_mfma_f32_16x16x32_bf16 v[74:77], v[182:185], v[206:209], v[74:77]
	v_mfma_f32_16x16x32_bf16 v[70:73], v[174:177], v[214:217], v[70:73]
	v_mfma_f32_16x16x32_bf16 v[66:69], v[182:185], v[214:217], v[66:69]
	s_barrier
	s_setprio 0
	s_add_i32 s30, s60, s38
	v_lshl_add_u64 v[146:147], v[146:147], 0, s[10:11]
	s_mov_b32 m0, s30
	ds_read_b128 v[186:189], v152 offset:49152
	ds_read_b128 v[190:193], v152 offset:50176
	ds_read_b128 v[194:197], v152 offset:51200
	ds_read_b128 v[198:201], v152 offset:52224
	ds_read_b128 v[202:205], v152 offset:53248
	ds_read_b128 v[206:209], v152 offset:54272
	ds_read_b128 v[210:213], v152 offset:55296
	ds_read_b128 v[214:217], v152 offset:56320
	global_load_lds_dwordx4 v[146:147], off
	s_add_i32 m0, s30, 0x2000
	s_add_u32 s28, s28, 0x160080
	v_lshl_add_u64 v[146:147], v[218:219], 0, s[10:11]
	s_addc_u32 s29, s29, 0
	s_add_i32 s30, s61, s38
	global_load_lds_dwordx4 v[146:147], off
	v_lshl_add_u64 v[146:147], s[28:29], 0, v[132:133]
	s_mov_b32 m0, s30
	s_nop 0
	global_load_lds_dwordx4 v[146:147], off
	v_lshl_add_u64 v[146:147], s[28:29], 0, v[136:137]
	s_add_i32 m0, s30, 0x2000
	s_nop 0
	global_load_lds_dwordx4 v[146:147], off
	v_lshl_add_u64 v[146:147], v[220:221], 0, s[10:11]
	s_mov_b32 m0, s44
	s_nop 0
	global_load_lds_dwordx4 v[146:147], off
	v_lshl_add_u64 v[146:147], v[222:223], 0, s[10:11]
	s_mov_b32 m0, s45
	s_nop 0
	global_load_lds_dwordx4 v[146:147], off
	s_waitcnt vmcnt(8)
	s_waitcnt lgkmcnt(0)
	s_setprio 1
	s_barrier
	v_mfma_f32_16x16x32_bf16 v[62:65], v[154:157], v[186:189], v[62:65]
	v_mfma_f32_16x16x32_bf16 v[58:61], v[162:165], v[186:189], v[58:61]
	v_mfma_f32_16x16x32_bf16 v[54:57], v[154:157], v[194:197], v[54:57]
	v_mfma_f32_16x16x32_bf16 v[46:49], v[162:165], v[194:197], v[46:49]
	v_mfma_f32_16x16x32_bf16 v[38:41], v[154:157], v[202:205], v[38:41]
	v_mfma_f32_16x16x32_bf16 v[30:33], v[162:165], v[202:205], v[30:33]
	v_mfma_f32_16x16x32_bf16 v[22:25], v[154:157], v[210:213], v[22:25]
	v_mfma_f32_16x16x32_bf16 v[14:17], v[162:165], v[210:213], v[14:17]
	v_mfma_f32_16x16x32_bf16 v[62:65], v[158:161], v[190:193], v[62:65]
	v_mfma_f32_16x16x32_bf16 v[58:61], v[166:169], v[190:193], v[58:61]
	v_mfma_f32_16x16x32_bf16 v[54:57], v[158:161], v[198:201], v[54:57]
	v_mfma_f32_16x16x32_bf16 v[46:49], v[166:169], v[198:201], v[46:49]
	v_mfma_f32_16x16x32_bf16 v[38:41], v[158:161], v[206:209], v[38:41]
	v_mfma_f32_16x16x32_bf16 v[30:33], v[166:169], v[206:209], v[30:33]
	v_mfma_f32_16x16x32_bf16 v[22:25], v[158:161], v[214:217], v[22:25]
	v_mfma_f32_16x16x32_bf16 v[14:17], v[166:169], v[214:217], v[14:17]
	s_setprio 0
	s_setprio 1
	v_mfma_f32_16x16x32_bf16 v[50:53], v[170:173], v[186:189], v[50:53]
	v_mfma_f32_16x16x32_bf16 v[42:45], v[178:181], v[186:189], v[42:45]
	v_mfma_f32_16x16x32_bf16 v[34:37], v[170:173], v[194:197], v[34:37]
	v_mfma_f32_16x16x32_bf16 v[26:29], v[178:181], v[194:197], v[26:29]
	v_mfma_f32_16x16x32_bf16 v[18:21], v[170:173], v[202:205], v[18:21]
	v_mfma_f32_16x16x32_bf16 v[10:13], v[178:181], v[202:205], v[10:13]
	v_mfma_f32_16x16x32_bf16 v[6:9], v[170:173], v[210:213], v[6:9]
	v_mfma_f32_16x16x32_bf16 v[2:5], v[178:181], v[210:213], v[2:5]
	v_mfma_f32_16x16x32_bf16 v[50:53], v[174:177], v[190:193], v[50:53]
	v_mfma_f32_16x16x32_bf16 v[42:45], v[182:185], v[190:193], v[42:45]
	v_mfma_f32_16x16x32_bf16 v[34:37], v[174:177], v[198:201], v[34:37]
	v_mfma_f32_16x16x32_bf16 v[26:29], v[182:185], v[198:201], v[26:29]
	v_mfma_f32_16x16x32_bf16 v[18:21], v[174:177], v[206:209], v[18:21]
	v_mfma_f32_16x16x32_bf16 v[10:13], v[182:185], v[206:209], v[10:13]
	v_mfma_f32_16x16x32_bf16 v[6:9], v[174:177], v[214:217], v[6:9]
	v_mfma_f32_16x16x32_bf16 v[2:5], v[182:185], v[214:217], v[2:5]
	s_barrier
	s_setprio 0
	s_add_i32 s59, s59, 2
	s_add_u32 s26, s26, 0x100
	s_addc_u32 s27, s27, 0
	s_add_u32 s57, s57, 0x100
	s_addc_u32 s58, s58, 0
	s_cmpk_gt_u32 s59, 0x55
	.p2alignl 6, 3212836864

.LBB0_1696:
	s_ashr_i32 s37, s36, 31
	s_lshl_b64 s[38:39], s[36:37], 20
	s_add_u32 s38, s20, s38
	s_addc_u32 s39, s21, s39
	s_and_b64 s[40:41], s[10:11], exec
	s_cselect_b32 s37, s39, s47
	s_cselect_b32 s43, s38, s46
	s_ashr_i32 s35, s34, 31
	s_lshl_b64 s[40:41], s[34:35], 20
	s_add_u32 s40, s23, s40
	s_addc_u32 s41, s33, s41
	s_and_b64 s[50:51], s[10:11], exec
	s_cselect_b32 s35, s41, s49
	s_cselect_b32 s45, s40, s48
	s_lshl_b32 s50, s44, 8
	s_ashr_i32 s51, s50, 31
	v_lshl_add_u64 v[238:239], s[50:51], 2, v[140:141]
	global_load_dword v240, v[238:239], off
	global_load_dword v242, v[238:239], off offset:64
	global_load_dword v244, v[238:239], off offset:128
	global_load_dword v246, v[238:239], off offset:192
	global_load_dword v248, v[238:239], off offset:512
	global_load_dword v250, v[238:239], off offset:576
	global_load_dword v252, v[238:239], off offset:640
	global_load_dword v238, v[238:239], off offset:704
	s_add_u32 s46, s46, 0x80080
	s_addc_u32 s47, s47, 0
	s_add_u32 s69, s48, 0x100
	s_addc_u32 s70, s49, 0
	s_mov_b32 s71, -2
	s_waitcnt vmcnt(0)
	ds_read_b128 v[156:159], v176
	ds_read_b128 v[160:163], v176 offset:1024
	ds_read_b128 v[164:167], v176 offset:2048
	ds_read_b128 v[168:171], v176 offset:3072
	ds_read_b128 v[180:183], v177
	ds_read_b128 v[184:187], v177 offset:1024
	ds_read_b128 v[188:191], v177 offset:2048
	ds_read_b128 v[192:195], v177 offset:3072
	s_add_u32 s48, s46, 0xfff80080
	s_addc_u32 s49, s47, -1
	s_cmp_eq_u32 s71, 28
	s_cselect_b32 s51, s37, s49
	s_cselect_b32 s50, s43, s48
	s_cselect_b32 s49, s35, s70
	s_cselect_b32 s48, s45, s69
	v_lshl_add_u64 v[172:173], s[46:47], 0, v[148:149]
	s_add_i32 m0, s53, 0xc000
	ds_read_b128 v[196:199], v178
	ds_read_b128 v[200:203], v178 offset:1024
	ds_read_b128 v[204:207], v178 offset:2048
	ds_read_b128 v[208:211], v178 offset:3072
	ds_read_b128 v[212:215], v178 offset:4096
	ds_read_b128 v[216:219], v178 offset:5120
	ds_read_b128 v[220:223], v178 offset:6144
	ds_read_b128 v[224:227], v178 offset:7168
	global_load_lds_dwordx4 v[172:173], off
	v_lshl_add_u64 v[172:173], s[46:47], 0, v[150:151]
	s_add_i32 m0, s53, 0xe000
	s_nop 0
	global_load_lds_dwordx4 v[172:173], off
	s_waitcnt vmcnt(8)
	s_waitcnt lgkmcnt(0)
	s_setprio 1
	s_barrier
	v_mfma_f32_16x16x32_bf16 v[126:129], v[156:159], v[196:199], 0
	v_mfma_f32_16x16x32_bf16 v[122:125], v[164:167], v[196:199], 0
	v_mfma_f32_16x16x32_bf16 v[118:121], v[156:159], v[204:207], 0
	v_mfma_f32_16x16x32_bf16 v[114:117], v[164:167], v[204:207], 0
	v_mfma_f32_16x16x32_bf16 v[110:113], v[156:159], v[212:215], 0
	v_mfma_f32_16x16x32_bf16 v[106:109], v[164:167], v[212:215], 0
	v_mfma_f32_16x16x32_bf16 v[102:105], v[156:159], v[220:223], 0
	v_mfma_f32_16x16x32_bf16 v[98:101], v[164:167], v[220:223], 0
	v_mfma_f32_16x16x32_bf16 v[126:129], v[160:163], v[200:203], v[126:129]
	v_mfma_f32_16x16x32_bf16 v[122:125], v[168:171], v[200:203], v[122:125]
	v_mfma_f32_16x16x32_bf16 v[118:121], v[160:163], v[208:211], v[118:121]
	v_mfma_f32_16x16x32_bf16 v[114:117], v[168:171], v[208:211], v[114:117]
	v_mfma_f32_16x16x32_bf16 v[110:113], v[160:163], v[216:219], v[110:113]
	v_mfma_f32_16x16x32_bf16 v[106:109], v[168:171], v[216:219], v[106:109]
	v_mfma_f32_16x16x32_bf16 v[102:105], v[160:163], v[224:227], v[102:105]
	v_mfma_f32_16x16x32_bf16 v[98:101], v[168:171], v[224:227], v[98:101]
	s_setprio 0
	s_setprio 1
	v_mfma_f32_16x16x32_bf16 v[38:41], v[180:183], v[196:199], 0
	v_mfma_f32_16x16x32_bf16 v[34:37], v[188:191], v[196:199], 0
	v_mfma_f32_16x16x32_bf16 v[46:49], v[180:183], v[204:207], 0
	v_mfma_f32_16x16x32_bf16 v[42:45], v[188:191], v[204:207], 0
	v_mfma_f32_16x16x32_bf16 v[54:57], v[180:183], v[212:215], 0
	v_mfma_f32_16x16x32_bf16 v[50:53], v[188:191], v[212:215], 0
	v_mfma_f32_16x16x32_bf16 v[62:65], v[180:183], v[220:223], 0
	v_mfma_f32_16x16x32_bf16 v[58:61], v[188:191], v[220:223], 0
	v_mfma_f32_16x16x32_bf16 v[38:41], v[184:187], v[200:203], v[38:41]
	v_mfma_f32_16x16x32_bf16 v[34:37], v[192:195], v[200:203], v[34:37]
	v_mfma_f32_16x16x32_bf16 v[46:49], v[184:187], v[208:211], v[46:49]
	v_mfma_f32_16x16x32_bf16 v[42:45], v[192:195], v[208:211], v[42:45]
	v_mfma_f32_16x16x32_bf16 v[54:57], v[184:187], v[216:219], v[54:57]
	v_mfma_f32_16x16x32_bf16 v[50:53], v[192:195], v[216:219], v[50:53]
	v_mfma_f32_16x16x32_bf16 v[62:65], v[184:187], v[224:227], v[62:65]
	v_mfma_f32_16x16x32_bf16 v[58:61], v[192:195], v[224:227], v[58:61]
	s_barrier
	s_setprio 0
	s_add_i32 s72, s65, s52
	v_lshl_add_u64 v[172:173], s[48:49], 0, v[132:133]
	s_mov_b32 m0, s72
	ds_read_b128 v[196:199], v178 offset:16384
	ds_read_b128 v[200:203], v178 offset:17408
	ds_read_b128 v[204:207], v178 offset:18432
	ds_read_b128 v[208:211], v178 offset:19456
	ds_read_b128 v[212:215], v178 offset:20480
	ds_read_b128 v[216:219], v178 offset:21504
	ds_read_b128 v[220:223], v178 offset:22528
	ds_read_b128 v[224:227], v178 offset:23552
	global_load_lds_dwordx4 v[172:173], off
	s_add_i32 m0, s72, 0x2000
	s_add_u32 s72, s48, 0x80000
	v_lshl_add_u64 v[228:229], s[48:49], 0, v[136:137]
	s_addc_u32 s73, s49, 0
	s_add_i32 s74, s66, s52
	global_load_lds_dwordx4 v[228:229], off
	v_lshl_add_u64 v[230:231], s[72:73], 0, v[132:133]
	s_mov_b32 m0, s74
	v_lshl_add_u64 v[232:233], s[50:51], 0, v[134:135]
	global_load_lds_dwordx4 v[230:231], off
	v_lshl_add_u64 v[230:231], s[72:73], 0, v[136:137]
	s_add_i32 m0, s74, 0x2000
	s_nop 0
	global_load_lds_dwordx4 v[230:231], off
	v_lshl_add_u64 v[230:231], s[50:51], 0, v[130:131]
	s_mov_b32 m0, s53
	s_nop 0
	global_load_lds_dwordx4 v[230:231], off
	s_mov_b32 m0, s54
	s_nop 0
	global_load_lds_dwordx4 v[232:233], off
	s_waitcnt vmcnt(8)
	s_waitcnt lgkmcnt(0)
	s_setprio 1
	s_barrier
	v_mfma_f32_16x16x32_bf16 v[94:97], v[156:159], v[196:199], 0
	v_mfma_f32_16x16x32_bf16 v[90:93], v[164:167], v[196:199], 0
	v_mfma_f32_16x16x32_bf16 v[86:89], v[156:159], v[204:207], 0
	v_mfma_f32_16x16x32_bf16 v[82:85], v[164:167], v[204:207], 0
	v_mfma_f32_16x16x32_bf16 v[78:81], v[156:159], v[212:215], 0
	v_mfma_f32_16x16x32_bf16 v[74:77], v[164:167], v[212:215], 0
	v_mfma_f32_16x16x32_bf16 v[70:73], v[156:159], v[220:223], 0
	v_mfma_f32_16x16x32_bf16 v[66:69], v[164:167], v[220:223], 0
	v_mfma_f32_16x16x32_bf16 v[94:97], v[160:163], v[200:203], v[94:97]
	v_mfma_f32_16x16x32_bf16 v[90:93], v[168:171], v[200:203], v[90:93]
	v_mfma_f32_16x16x32_bf16 v[86:89], v[160:163], v[208:211], v[86:89]
	v_mfma_f32_16x16x32_bf16 v[82:85], v[168:171], v[208:211], v[82:85]
	v_mfma_f32_16x16x32_bf16 v[78:81], v[160:163], v[216:219], v[78:81]
	v_mfma_f32_16x16x32_bf16 v[74:77], v[168:171], v[216:219], v[74:77]
	v_mfma_f32_16x16x32_bf16 v[70:73], v[160:163], v[224:227], v[70:73]
	v_mfma_f32_16x16x32_bf16 v[66:69], v[168:171], v[224:227], v[66:69]
	s_setprio 0
	s_setprio 1
	v_mfma_f32_16x16x32_bf16 v[6:9], v[180:183], v[196:199], 0
	v_mfma_f32_16x16x32_bf16 v[2:5], v[188:191], v[196:199], 0
	v_mfma_f32_16x16x32_bf16 v[18:21], v[180:183], v[204:207], 0
	v_mfma_f32_16x16x32_bf16 v[14:17], v[188:191], v[204:207], 0
	v_mfma_f32_16x16x32_bf16 v[26:29], v[180:183], v[212:215], 0
	v_mfma_f32_16x16x32_bf16 v[22:25], v[188:191], v[212:215], 0
	v_mfma_f32_16x16x32_bf16 v[30:33], v[180:183], v[220:223], 0
	v_mfma_f32_16x16x32_bf16 v[10:13], v[188:191], v[220:223], 0
	v_mfma_f32_16x16x32_bf16 v[6:9], v[184:187], v[200:203], v[6:9]
	v_mfma_f32_16x16x32_bf16 v[2:5], v[192:195], v[200:203], v[2:5]
	v_mfma_f32_16x16x32_bf16 v[18:21], v[184:187], v[208:211], v[18:21]
	v_mfma_f32_16x16x32_bf16 v[14:17], v[192:195], v[208:211], v[14:17]
	v_mfma_f32_16x16x32_bf16 v[26:29], v[184:187], v[216:219], v[26:29]
	v_mfma_f32_16x16x32_bf16 v[22:25], v[192:195], v[216:219], v[22:25]
	v_mfma_f32_16x16x32_bf16 v[30:33], v[184:187], v[224:227], v[30:33]
	v_mfma_f32_16x16x32_bf16 v[10:13], v[192:195], v[224:227], v[10:13]
	s_barrier
	s_setprio 0
	s_add_i32 s72, 0, 0x18000
	v_add_u32_e32 v138, s72, v174
	s_add_i32 s73, 0, 0x1c000
	ds_read_b128 v[156:159], v138
	ds_read_b128 v[160:163], v138 offset:1024
	ds_read_b128 v[164:167], v138 offset:2048
	ds_read_b128 v[168:171], v138 offset:3072
	v_add_u32_e32 v138, s73, v174
	ds_read_b128 v[180:183], v138
	ds_read_b128 v[184:187], v138 offset:1024
	ds_read_b128 v[188:191], v138 offset:2048
	ds_read_b128 v[192:195], v138 offset:3072
	s_add_u32 s50, s50, 0x80000
	s_addc_u32 s51, s51, 0
	s_mov_b32 m0, s55
	v_lshl_add_u64 v[234:235], s[50:51], 0, v[130:131]
	ds_read_b128 v[196:199], v178 offset:32768
	ds_read_b128 v[200:203], v178 offset:33792
	ds_read_b128 v[204:207], v178 offset:34816
	ds_read_b128 v[208:211], v178 offset:35840
	ds_read_b128 v[212:215], v178 offset:36864
	ds_read_b128 v[216:219], v178 offset:37888
	ds_read_b128 v[220:223], v178 offset:38912
	ds_read_b128 v[224:227], v178 offset:39936
	global_load_lds_dwordx4 v[234:235], off
	v_lshl_add_u64 v[234:235], s[50:51], 0, v[134:135]
	s_mov_b32 m0, s56
	s_nop 0
	global_load_lds_dwordx4 v[234:235], off
	s_waitcnt vmcnt(8)
	s_waitcnt lgkmcnt(0)
	s_setprio 1
	s_barrier
	v_mfma_f32_16x16x32_bf16 v[126:129], v[156:159], v[196:199], v[126:129]
	v_mfma_f32_16x16x32_bf16 v[122:125], v[164:167], v[196:199], v[122:125]
	v_mfma_f32_16x16x32_bf16 v[118:121], v[156:159], v[204:207], v[118:121]
	v_mfma_f32_16x16x32_bf16 v[114:117], v[164:167], v[204:207], v[114:117]
	v_mfma_f32_16x16x32_bf16 v[110:113], v[156:159], v[212:215], v[110:113]
	v_mfma_f32_16x16x32_bf16 v[106:109], v[164:167], v[212:215], v[106:109]
	v_mfma_f32_16x16x32_bf16 v[102:105], v[156:159], v[220:223], v[102:105]
	v_mfma_f32_16x16x32_bf16 v[98:101], v[164:167], v[220:223], v[98:101]
	v_mfma_f32_16x16x32_bf16 v[126:129], v[160:163], v[200:203], v[126:129]
	v_mfma_f32_16x16x32_bf16 v[122:125], v[168:171], v[200:203], v[122:125]
	v_mfma_f32_16x16x32_bf16 v[118:121], v[160:163], v[208:211], v[118:121]
	v_mfma_f32_16x16x32_bf16 v[114:117], v[168:171], v[208:211], v[114:117]
	v_mfma_f32_16x16x32_bf16 v[110:113], v[160:163], v[216:219], v[110:113]
	v_mfma_f32_16x16x32_bf16 v[106:109], v[168:171], v[216:219], v[106:109]
	v_mfma_f32_16x16x32_bf16 v[102:105], v[160:163], v[224:227], v[102:105]
	v_mfma_f32_16x16x32_bf16 v[98:101], v[168:171], v[224:227], v[98:101]
	s_setprio 0
	s_setprio 1
	v_mfma_f32_16x16x32_bf16 v[38:41], v[180:183], v[196:199], v[38:41]
	v_mfma_f32_16x16x32_bf16 v[34:37], v[188:191], v[196:199], v[34:37]
	v_mfma_f32_16x16x32_bf16 v[46:49], v[180:183], v[204:207], v[46:49]
	v_mfma_f32_16x16x32_bf16 v[42:45], v[188:191], v[204:207], v[42:45]
	v_mfma_f32_16x16x32_bf16 v[54:57], v[180:183], v[212:215], v[54:57]
	v_mfma_f32_16x16x32_bf16 v[50:53], v[188:191], v[212:215], v[50:53]
	v_mfma_f32_16x16x32_bf16 v[62:65], v[180:183], v[220:223], v[62:65]
	v_mfma_f32_16x16x32_bf16 v[58:61], v[188:191], v[220:223], v[58:61]
	v_mfma_f32_16x16x32_bf16 v[38:41], v[184:187], v[200:203], v[38:41]
	v_mfma_f32_16x16x32_bf16 v[34:37], v[192:195], v[200:203], v[34:37]
	v_mfma_f32_16x16x32_bf16 v[46:49], v[184:187], v[208:211], v[46:49]
	v_mfma_f32_16x16x32_bf16 v[42:45], v[192:195], v[208:211], v[42:45]
	v_mfma_f32_16x16x32_bf16 v[54:57], v[184:187], v[216:219], v[54:57]
	v_mfma_f32_16x16x32_bf16 v[50:53], v[192:195], v[216:219], v[50:53]
	v_mfma_f32_16x16x32_bf16 v[62:65], v[184:187], v[224:227], v[62:65]
	v_mfma_f32_16x16x32_bf16 v[58:61], v[192:195], v[224:227], v[58:61]
	s_barrier
	s_setprio 0
	s_add_i32 s50, s72, s52
	v_lshl_add_u64 v[172:173], v[172:173], 0, s[6:7]
	s_mov_b32 m0, s50
	ds_read_b128 v[196:199], v178 offset:49152
	ds_read_b128 v[200:203], v178 offset:50176
	ds_read_b128 v[204:207], v178 offset:51200
	ds_read_b128 v[208:211], v178 offset:52224
	ds_read_b128 v[212:215], v178 offset:53248
	ds_read_b128 v[216:219], v178 offset:54272
	ds_read_b128 v[220:223], v178 offset:55296
	ds_read_b128 v[224:227], v178 offset:56320
	global_load_lds_dwordx4 v[172:173], off
	s_add_i32 m0, s50, 0x2000
	s_add_u32 s48, s48, 0x80080
	v_lshl_add_u64 v[172:173], v[228:229], 0, s[6:7]
	s_addc_u32 s49, s49, 0
	s_add_i32 s50, s73, s52
	global_load_lds_dwordx4 v[172:173], off
	v_lshl_add_u64 v[172:173], s[48:49], 0, v[132:133]
	s_mov_b32 m0, s50
	s_nop 0
	global_load_lds_dwordx4 v[172:173], off
	v_lshl_add_u64 v[172:173], s[48:49], 0, v[136:137]
	s_add_i32 m0, s50, 0x2000
	s_nop 0
	global_load_lds_dwordx4 v[172:173], off
	v_lshl_add_u64 v[172:173], v[230:231], 0, s[6:7]
	s_mov_b32 m0, s61
	s_nop 0
	global_load_lds_dwordx4 v[172:173], off
	v_lshl_add_u64 v[172:173], v[232:233], 0, s[6:7]
	s_mov_b32 m0, s62
	s_nop 0
	global_load_lds_dwordx4 v[172:173], off
	s_waitcnt vmcnt(8)
	s_waitcnt lgkmcnt(0)
	s_setprio 1
	s_barrier
	v_mfma_f32_16x16x32_bf16 v[94:97], v[156:159], v[196:199], v[94:97]
	v_mfma_f32_16x16x32_bf16 v[90:93], v[164:167], v[196:199], v[90:93]
	v_mfma_f32_16x16x32_bf16 v[86:89], v[156:159], v[204:207], v[86:89]
	v_mfma_f32_16x16x32_bf16 v[82:85], v[164:167], v[204:207], v[82:85]
	v_mfma_f32_16x16x32_bf16 v[78:81], v[156:159], v[212:215], v[78:81]
	v_mfma_f32_16x16x32_bf16 v[74:77], v[164:167], v[212:215], v[74:77]
	v_mfma_f32_16x16x32_bf16 v[70:73], v[156:159], v[220:223], v[70:73]
	v_mfma_f32_16x16x32_bf16 v[66:69], v[164:167], v[220:223], v[66:69]
	v_mfma_f32_16x16x32_bf16 v[94:97], v[160:163], v[200:203], v[94:97]
	v_mfma_f32_16x16x32_bf16 v[90:93], v[168:171], v[200:203], v[90:93]
	v_mfma_f32_16x16x32_bf16 v[86:89], v[160:163], v[208:211], v[86:89]
	v_mfma_f32_16x16x32_bf16 v[82:85], v[168:171], v[208:211], v[82:85]
	v_mfma_f32_16x16x32_bf16 v[78:81], v[160:163], v[216:219], v[78:81]
	v_mfma_f32_16x16x32_bf16 v[74:77], v[168:171], v[216:219], v[74:77]
	v_mfma_f32_16x16x32_bf16 v[70:73], v[160:163], v[224:227], v[70:73]
	v_mfma_f32_16x16x32_bf16 v[66:69], v[168:171], v[224:227], v[66:69]
	s_setprio 0
	s_setprio 1
	v_mfma_f32_16x16x32_bf16 v[6:9], v[180:183], v[196:199], v[6:9]
	v_mfma_f32_16x16x32_bf16 v[2:5], v[188:191], v[196:199], v[2:5]
	v_mfma_f32_16x16x32_bf16 v[18:21], v[180:183], v[204:207], v[18:21]
	v_mfma_f32_16x16x32_bf16 v[14:17], v[188:191], v[204:207], v[14:17]
	v_mfma_f32_16x16x32_bf16 v[26:29], v[180:183], v[212:215], v[26:29]
	v_mfma_f32_16x16x32_bf16 v[22:25], v[188:191], v[212:215], v[22:25]
	v_mfma_f32_16x16x32_bf16 v[30:33], v[180:183], v[220:223], v[30:33]
	v_mfma_f32_16x16x32_bf16 v[10:13], v[188:191], v[220:223], v[10:13]
	v_mfma_f32_16x16x32_bf16 v[6:9], v[184:187], v[200:203], v[6:9]
	v_mfma_f32_16x16x32_bf16 v[2:5], v[192:195], v[200:203], v[2:5]
	v_mfma_f32_16x16x32_bf16 v[18:21], v[184:187], v[208:211], v[18:21]
	v_mfma_f32_16x16x32_bf16 v[14:17], v[192:195], v[208:211], v[14:17]
	v_mfma_f32_16x16x32_bf16 v[26:29], v[184:187], v[216:219], v[26:29]
	v_mfma_f32_16x16x32_bf16 v[22:25], v[192:195], v[216:219], v[22:25]
	v_mfma_f32_16x16x32_bf16 v[30:33], v[184:187], v[224:227], v[30:33]
	v_mfma_f32_16x16x32_bf16 v[10:13], v[192:195], v[224:227], v[10:13]
	s_barrier
	s_setprio 0
	s_add_i32 s71, s71, 2
	s_add_u32 s46, s46, 0x100
	s_addc_u32 s47, s47, 0
	s_add_u32 s69, s69, 0x100
	s_addc_u32 s70, s70, 0
	s_cmp_gt_u32 s71, 29
	.p2alignl 6, 3212836864

.LBB0_2113:
	s_ashr_i32 s25, s24, 31
	s_lshl_b64 s[26:27], s[24:25], 20
	v_readlane_b32 s28, v254, 22
	v_readlane_b32 s29, v254, 23
	s_add_u32 s26, s28, s26
	s_addc_u32 s27, s29, s27
	s_and_b64 s[28:29], s[4:5], exec
	s_cselect_b32 s25, s27, s35
	s_cselect_b32 s57, s26, s34
	s_ashr_i32 s23, s22, 31
	s_lshl_b64 s[28:29], s[22:23], 20
	s_add_u32 s28, s40, s28
	s_addc_u32 s29, s41, s29
	s_and_b64 s[38:39], s[4:5], exec
	s_cselect_b32 s23, s29, s37
	s_cselect_b32 s58, s28, s36
	s_add_u32 s34, s34, 0x80080
	s_addc_u32 s35, s35, 0
	s_add_u32 s59, s36, 0x100
	s_addc_u32 s60, s37, 0
	s_mov_b32 s61, -2
	ds_read_b128 v[154:157], v150
	ds_read_b128 v[158:161], v150 offset:1024
	ds_read_b128 v[162:165], v150 offset:2048
	ds_read_b128 v[166:169], v150 offset:3072
	ds_read_b128 v[170:173], v151
	ds_read_b128 v[174:177], v151 offset:1024
	ds_read_b128 v[178:181], v151 offset:2048
	ds_read_b128 v[182:185], v151 offset:3072
	s_add_u32 s36, s34, 0xfff80080
	s_addc_u32 s37, s35, -1
	s_cmp_eq_u32 s61, 28
	s_cselect_b32 s39, s25, s37
	s_cselect_b32 s38, s57, s36
	s_cselect_b32 s37, s23, s60
	s_cselect_b32 s36, s58, s59
	v_lshl_add_u64 v[146:147], s[34:35], 0, v[138:139]
	s_add_i32 m0, s31, 0xc000
	ds_read_b128 v[186:189], v152
	ds_read_b128 v[190:193], v152 offset:1024
	ds_read_b128 v[194:197], v152 offset:2048
	ds_read_b128 v[198:201], v152 offset:3072
	ds_read_b128 v[202:205], v152 offset:4096
	ds_read_b128 v[206:209], v152 offset:5120
	ds_read_b128 v[210:213], v152 offset:6144
	ds_read_b128 v[214:217], v152 offset:7168
	global_load_lds_dwordx4 v[146:147], off
	v_lshl_add_u64 v[146:147], s[34:35], 0, v[140:141]
	s_add_i32 m0, s31, 0xe000
	s_nop 0
	global_load_lds_dwordx4 v[146:147], off
	s_waitcnt vmcnt(8)
	s_waitcnt lgkmcnt(0)
	s_setprio 1
	s_barrier
	v_mfma_f32_16x16x32_bf16 v[126:129], v[154:157], v[186:189], 0
	v_mfma_f32_16x16x32_bf16 v[122:125], v[162:165], v[186:189], 0
	v_mfma_f32_16x16x32_bf16 v[118:121], v[154:157], v[194:197], 0
	v_mfma_f32_16x16x32_bf16 v[110:113], v[162:165], v[194:197], 0
	v_mfma_f32_16x16x32_bf16 v[102:105], v[154:157], v[202:205], 0
	v_mfma_f32_16x16x32_bf16 v[94:97], v[162:165], v[202:205], 0
	v_mfma_f32_16x16x32_bf16 v[86:89], v[154:157], v[210:213], 0
	v_mfma_f32_16x16x32_bf16 v[78:81], v[162:165], v[210:213], 0
	v_mfma_f32_16x16x32_bf16 v[126:129], v[158:161], v[190:193], v[126:129]
	v_mfma_f32_16x16x32_bf16 v[122:125], v[166:169], v[190:193], v[122:125]
	v_mfma_f32_16x16x32_bf16 v[118:121], v[158:161], v[198:201], v[118:121]
	v_mfma_f32_16x16x32_bf16 v[110:113], v[166:169], v[198:201], v[110:113]
	v_mfma_f32_16x16x32_bf16 v[102:105], v[158:161], v[206:209], v[102:105]
	v_mfma_f32_16x16x32_bf16 v[94:97], v[166:169], v[206:209], v[94:97]
	v_mfma_f32_16x16x32_bf16 v[86:89], v[158:161], v[214:217], v[86:89]
	v_mfma_f32_16x16x32_bf16 v[78:81], v[166:169], v[214:217], v[78:81]
	s_setprio 0
	s_setprio 1
	v_mfma_f32_16x16x32_bf16 v[114:117], v[170:173], v[186:189], 0
	v_mfma_f32_16x16x32_bf16 v[106:109], v[178:181], v[186:189], 0
	v_mfma_f32_16x16x32_bf16 v[98:101], v[170:173], v[194:197], 0
	v_mfma_f32_16x16x32_bf16 v[90:93], v[178:181], v[194:197], 0
	v_mfma_f32_16x16x32_bf16 v[82:85], v[170:173], v[202:205], 0
	v_mfma_f32_16x16x32_bf16 v[74:77], v[178:181], v[202:205], 0
	v_mfma_f32_16x16x32_bf16 v[70:73], v[170:173], v[210:213], 0
	v_mfma_f32_16x16x32_bf16 v[66:69], v[178:181], v[210:213], 0
	v_mfma_f32_16x16x32_bf16 v[114:117], v[174:177], v[190:193], v[114:117]
	v_mfma_f32_16x16x32_bf16 v[106:109], v[182:185], v[190:193], v[106:109]
	v_mfma_f32_16x16x32_bf16 v[98:101], v[174:177], v[198:201], v[98:101]
	v_mfma_f32_16x16x32_bf16 v[90:93], v[182:185], v[198:201], v[90:93]
	v_mfma_f32_16x16x32_bf16 v[82:85], v[174:177], v[206:209], v[82:85]
	v_mfma_f32_16x16x32_bf16 v[74:77], v[182:185], v[206:209], v[74:77]
	v_mfma_f32_16x16x32_bf16 v[70:73], v[174:177], v[214:217], v[70:73]
	v_mfma_f32_16x16x32_bf16 v[66:69], v[182:185], v[214:217], v[66:69]
	s_barrier
	s_setprio 0
	s_add_i32 s62, s50, s42
	v_lshl_add_u64 v[146:147], s[36:37], 0, v[132:133]
	s_mov_b32 m0, s62
	ds_read_b128 v[186:189], v152 offset:16384
	ds_read_b128 v[190:193], v152 offset:17408
	ds_read_b128 v[194:197], v152 offset:18432
	ds_read_b128 v[198:201], v152 offset:19456
	ds_read_b128 v[202:205], v152 offset:20480
	ds_read_b128 v[206:209], v152 offset:21504
	ds_read_b128 v[210:213], v152 offset:22528
	ds_read_b128 v[214:217], v152 offset:23552
	global_load_lds_dwordx4 v[146:147], off
	s_add_i32 m0, s62, 0x2000
	s_add_u32 s62, s36, 0x80000
	v_lshl_add_u64 v[218:219], s[36:37], 0, v[136:137]
	s_addc_u32 s63, s37, 0
	s_add_i32 s64, s51, s42
	global_load_lds_dwordx4 v[218:219], off
	v_lshl_add_u64 v[220:221], s[62:63], 0, v[132:133]
	s_mov_b32 m0, s64
	v_lshl_add_u64 v[222:223], s[38:39], 0, v[134:135]
	global_load_lds_dwordx4 v[220:221], off
	v_lshl_add_u64 v[220:221], s[62:63], 0, v[136:137]
	s_add_i32 m0, s64, 0x2000
	s_nop 0
	global_load_lds_dwordx4 v[220:221], off
	v_lshl_add_u64 v[220:221], s[38:39], 0, v[130:131]
	s_mov_b32 m0, s31
	s_nop 0
	global_load_lds_dwordx4 v[220:221], off
	s_mov_b32 m0, s43
	s_nop 0
	global_load_lds_dwordx4 v[222:223], off
	s_waitcnt vmcnt(8)
	s_waitcnt lgkmcnt(0)
	s_setprio 1
	s_barrier
	v_mfma_f32_16x16x32_bf16 v[62:65], v[154:157], v[186:189], 0
	v_mfma_f32_16x16x32_bf16 v[58:61], v[162:165], v[186:189], 0
	v_mfma_f32_16x16x32_bf16 v[54:57], v[154:157], v[194:197], 0
	v_mfma_f32_16x16x32_bf16 v[46:49], v[162:165], v[194:197], 0
	v_mfma_f32_16x16x32_bf16 v[38:41], v[154:157], v[202:205], 0
	v_mfma_f32_16x16x32_bf16 v[30:33], v[162:165], v[202:205], 0
	v_mfma_f32_16x16x32_bf16 v[22:25], v[154:157], v[210:213], 0
	v_mfma_f32_16x16x32_bf16 v[14:17], v[162:165], v[210:213], 0
	v_mfma_f32_16x16x32_bf16 v[62:65], v[158:161], v[190:193], v[62:65]
	v_mfma_f32_16x16x32_bf16 v[58:61], v[166:169], v[190:193], v[58:61]
	v_mfma_f32_16x16x32_bf16 v[54:57], v[158:161], v[198:201], v[54:57]
	v_mfma_f32_16x16x32_bf16 v[46:49], v[166:169], v[198:201], v[46:49]
	v_mfma_f32_16x16x32_bf16 v[38:41], v[158:161], v[206:209], v[38:41]
	v_mfma_f32_16x16x32_bf16 v[30:33], v[166:169], v[206:209], v[30:33]
	v_mfma_f32_16x16x32_bf16 v[22:25], v[158:161], v[214:217], v[22:25]
	v_mfma_f32_16x16x32_bf16 v[14:17], v[166:169], v[214:217], v[14:17]
	s_setprio 0
	s_setprio 1
	v_mfma_f32_16x16x32_bf16 v[50:53], v[170:173], v[186:189], 0
	v_mfma_f32_16x16x32_bf16 v[42:45], v[178:181], v[186:189], 0
	v_mfma_f32_16x16x32_bf16 v[34:37], v[170:173], v[194:197], 0
	v_mfma_f32_16x16x32_bf16 v[26:29], v[178:181], v[194:197], 0
	v_mfma_f32_16x16x32_bf16 v[18:21], v[170:173], v[202:205], 0
	v_mfma_f32_16x16x32_bf16 v[10:13], v[178:181], v[202:205], 0
	v_mfma_f32_16x16x32_bf16 v[6:9], v[170:173], v[210:213], 0
	v_mfma_f32_16x16x32_bf16 v[2:5], v[178:181], v[210:213], 0
	v_mfma_f32_16x16x32_bf16 v[50:53], v[174:177], v[190:193], v[50:53]
	v_mfma_f32_16x16x32_bf16 v[42:45], v[182:185], v[190:193], v[42:45]
	v_mfma_f32_16x16x32_bf16 v[34:37], v[174:177], v[198:201], v[34:37]
	v_mfma_f32_16x16x32_bf16 v[26:29], v[182:185], v[198:201], v[26:29]
	v_mfma_f32_16x16x32_bf16 v[18:21], v[174:177], v[206:209], v[18:21]
	v_mfma_f32_16x16x32_bf16 v[10:13], v[182:185], v[206:209], v[10:13]
	v_mfma_f32_16x16x32_bf16 v[6:9], v[174:177], v[214:217], v[6:9]
	v_mfma_f32_16x16x32_bf16 v[2:5], v[182:185], v[214:217], v[2:5]
	s_barrier
	s_setprio 0
	s_add_i32 s62, 0, 0x18000
	v_add_u32_e32 v153, s62, v148
	s_add_i32 s63, 0, 0x1c000
	ds_read_b128 v[154:157], v153
	ds_read_b128 v[158:161], v153 offset:1024
	ds_read_b128 v[162:165], v153 offset:2048
	ds_read_b128 v[166:169], v153 offset:3072
	v_add_u32_e32 v153, s63, v148
	ds_read_b128 v[170:173], v153
	ds_read_b128 v[174:177], v153 offset:1024
	ds_read_b128 v[178:181], v153 offset:2048
	ds_read_b128 v[182:185], v153 offset:3072
	s_add_u32 s38, s38, 0x80000
	s_addc_u32 s39, s39, 0
	s_mov_b32 m0, s44
	v_lshl_add_u64 v[224:225], s[38:39], 0, v[130:131]
	ds_read_b128 v[186:189], v152 offset:32768
	ds_read_b128 v[190:193], v152 offset:33792
	ds_read_b128 v[194:197], v152 offset:34816
	ds_read_b128 v[198:201], v152 offset:35840
	ds_read_b128 v[202:205], v152 offset:36864
	ds_read_b128 v[206:209], v152 offset:37888
	ds_read_b128 v[210:213], v152 offset:38912
	ds_read_b128 v[214:217], v152 offset:39936
	global_load_lds_dwordx4 v[224:225], off
	v_lshl_add_u64 v[224:225], s[38:39], 0, v[134:135]
	s_mov_b32 m0, s45
	s_nop 0
	global_load_lds_dwordx4 v[224:225], off
	s_waitcnt vmcnt(8)
	s_waitcnt lgkmcnt(0)
	s_setprio 1
	s_barrier
	v_mfma_f32_16x16x32_bf16 v[126:129], v[154:157], v[186:189], v[126:129]
	v_mfma_f32_16x16x32_bf16 v[122:125], v[162:165], v[186:189], v[122:125]
	v_mfma_f32_16x16x32_bf16 v[118:121], v[154:157], v[194:197], v[118:121]
	v_mfma_f32_16x16x32_bf16 v[110:113], v[162:165], v[194:197], v[110:113]
	v_mfma_f32_16x16x32_bf16 v[102:105], v[154:157], v[202:205], v[102:105]
	v_mfma_f32_16x16x32_bf16 v[94:97], v[162:165], v[202:205], v[94:97]
	v_mfma_f32_16x16x32_bf16 v[86:89], v[154:157], v[210:213], v[86:89]
	v_mfma_f32_16x16x32_bf16 v[78:81], v[162:165], v[210:213], v[78:81]
	v_mfma_f32_16x16x32_bf16 v[126:129], v[158:161], v[190:193], v[126:129]
	v_mfma_f32_16x16x32_bf16 v[122:125], v[166:169], v[190:193], v[122:125]
	v_mfma_f32_16x16x32_bf16 v[118:121], v[158:161], v[198:201], v[118:121]
	v_mfma_f32_16x16x32_bf16 v[110:113], v[166:169], v[198:201], v[110:113]
	v_mfma_f32_16x16x32_bf16 v[102:105], v[158:161], v[206:209], v[102:105]
	v_mfma_f32_16x16x32_bf16 v[94:97], v[166:169], v[206:209], v[94:97]
	v_mfma_f32_16x16x32_bf16 v[86:89], v[158:161], v[214:217], v[86:89]
	v_mfma_f32_16x16x32_bf16 v[78:81], v[166:169], v[214:217], v[78:81]
	s_setprio 0
	s_setprio 1
	v_mfma_f32_16x16x32_bf16 v[114:117], v[170:173], v[186:189], v[114:117]
	v_mfma_f32_16x16x32_bf16 v[106:109], v[178:181], v[186:189], v[106:109]
	v_mfma_f32_16x16x32_bf16 v[98:101], v[170:173], v[194:197], v[98:101]
	v_mfma_f32_16x16x32_bf16 v[90:93], v[178:181], v[194:197], v[90:93]
	v_mfma_f32_16x16x32_bf16 v[82:85], v[170:173], v[202:205], v[82:85]
	v_mfma_f32_16x16x32_bf16 v[74:77], v[178:181], v[202:205], v[74:77]
	v_mfma_f32_16x16x32_bf16 v[70:73], v[170:173], v[210:213], v[70:73]
	v_mfma_f32_16x16x32_bf16 v[66:69], v[178:181], v[210:213], v[66:69]
	v_mfma_f32_16x16x32_bf16 v[114:117], v[174:177], v[190:193], v[114:117]
	v_mfma_f32_16x16x32_bf16 v[106:109], v[182:185], v[190:193], v[106:109]
	v_mfma_f32_16x16x32_bf16 v[98:101], v[174:177], v[198:201], v[98:101]
	v_mfma_f32_16x16x32_bf16 v[90:93], v[182:185], v[198:201], v[90:93]
	v_mfma_f32_16x16x32_bf16 v[82:85], v[174:177], v[206:209], v[82:85]
	v_mfma_f32_16x16x32_bf16 v[74:77], v[182:185], v[206:209], v[74:77]
	v_mfma_f32_16x16x32_bf16 v[70:73], v[174:177], v[214:217], v[70:73]
	v_mfma_f32_16x16x32_bf16 v[66:69], v[182:185], v[214:217], v[66:69]
	s_barrier
	s_setprio 0
	s_add_i32 s38, s62, s42
	v_lshl_add_u64 v[146:147], v[146:147], 0, s[10:11]
	s_mov_b32 m0, s38
	ds_read_b128 v[186:189], v152 offset:49152
	ds_read_b128 v[190:193], v152 offset:50176
	ds_read_b128 v[194:197], v152 offset:51200
	ds_read_b128 v[198:201], v152 offset:52224
	ds_read_b128 v[202:205], v152 offset:53248
	ds_read_b128 v[206:209], v152 offset:54272
	ds_read_b128 v[210:213], v152 offset:55296
	ds_read_b128 v[214:217], v152 offset:56320
	global_load_lds_dwordx4 v[146:147], off
	s_add_i32 m0, s38, 0x2000
	s_add_u32 s36, s36, 0x80080
	v_lshl_add_u64 v[146:147], v[218:219], 0, s[10:11]
	s_addc_u32 s37, s37, 0
	s_add_i32 s38, s63, s42
	global_load_lds_dwordx4 v[146:147], off
	v_lshl_add_u64 v[146:147], s[36:37], 0, v[132:133]
	s_mov_b32 m0, s38
	s_nop 0
	global_load_lds_dwordx4 v[146:147], off
	v_lshl_add_u64 v[146:147], s[36:37], 0, v[136:137]
	s_add_i32 m0, s38, 0x2000
	s_nop 0
	global_load_lds_dwordx4 v[146:147], off
	v_lshl_add_u64 v[146:147], v[220:221], 0, s[10:11]
	s_mov_b32 m0, s47
	s_nop 0
	global_load_lds_dwordx4 v[146:147], off
	v_lshl_add_u64 v[146:147], v[222:223], 0, s[10:11]
	s_mov_b32 m0, s48
	s_nop 0
	global_load_lds_dwordx4 v[146:147], off
	s_waitcnt vmcnt(8)
	s_waitcnt lgkmcnt(0)
	s_setprio 1
	s_barrier
	v_mfma_f32_16x16x32_bf16 v[62:65], v[154:157], v[186:189], v[62:65]
	v_mfma_f32_16x16x32_bf16 v[58:61], v[162:165], v[186:189], v[58:61]
	v_mfma_f32_16x16x32_bf16 v[54:57], v[154:157], v[194:197], v[54:57]
	v_mfma_f32_16x16x32_bf16 v[46:49], v[162:165], v[194:197], v[46:49]
	v_mfma_f32_16x16x32_bf16 v[38:41], v[154:157], v[202:205], v[38:41]
	v_mfma_f32_16x16x32_bf16 v[30:33], v[162:165], v[202:205], v[30:33]
	v_mfma_f32_16x16x32_bf16 v[22:25], v[154:157], v[210:213], v[22:25]
	v_mfma_f32_16x16x32_bf16 v[14:17], v[162:165], v[210:213], v[14:17]
	v_mfma_f32_16x16x32_bf16 v[62:65], v[158:161], v[190:193], v[62:65]
	v_mfma_f32_16x16x32_bf16 v[58:61], v[166:169], v[190:193], v[58:61]
	v_mfma_f32_16x16x32_bf16 v[54:57], v[158:161], v[198:201], v[54:57]
	v_mfma_f32_16x16x32_bf16 v[46:49], v[166:169], v[198:201], v[46:49]
	v_mfma_f32_16x16x32_bf16 v[38:41], v[158:161], v[206:209], v[38:41]
	v_mfma_f32_16x16x32_bf16 v[30:33], v[166:169], v[206:209], v[30:33]
	v_mfma_f32_16x16x32_bf16 v[22:25], v[158:161], v[214:217], v[22:25]
	v_mfma_f32_16x16x32_bf16 v[14:17], v[166:169], v[214:217], v[14:17]
	s_setprio 0
	s_setprio 1
	v_mfma_f32_16x16x32_bf16 v[50:53], v[170:173], v[186:189], v[50:53]
	v_mfma_f32_16x16x32_bf16 v[42:45], v[178:181], v[186:189], v[42:45]
	v_mfma_f32_16x16x32_bf16 v[34:37], v[170:173], v[194:197], v[34:37]
	v_mfma_f32_16x16x32_bf16 v[26:29], v[178:181], v[194:197], v[26:29]
	v_mfma_f32_16x16x32_bf16 v[18:21], v[170:173], v[202:205], v[18:21]
	v_mfma_f32_16x16x32_bf16 v[10:13], v[178:181], v[202:205], v[10:13]
	v_mfma_f32_16x16x32_bf16 v[6:9], v[170:173], v[210:213], v[6:9]
	v_mfma_f32_16x16x32_bf16 v[2:5], v[178:181], v[210:213], v[2:5]
	v_mfma_f32_16x16x32_bf16 v[50:53], v[174:177], v[190:193], v[50:53]
	v_mfma_f32_16x16x32_bf16 v[42:45], v[182:185], v[190:193], v[42:45]
	v_mfma_f32_16x16x32_bf16 v[34:37], v[174:177], v[198:201], v[34:37]
	v_mfma_f32_16x16x32_bf16 v[26:29], v[182:185], v[198:201], v[26:29]
	v_mfma_f32_16x16x32_bf16 v[18:21], v[174:177], v[206:209], v[18:21]
	v_mfma_f32_16x16x32_bf16 v[10:13], v[182:185], v[206:209], v[10:13]
	v_mfma_f32_16x16x32_bf16 v[6:9], v[174:177], v[214:217], v[6:9]
	v_mfma_f32_16x16x32_bf16 v[2:5], v[182:185], v[214:217], v[2:5]
	s_barrier
	s_setprio 0
	s_add_i32 s61, s61, 2
	s_add_u32 s34, s34, 0x100
	s_addc_u32 s35, s35, 0
	s_add_u32 s59, s59, 0x100
	s_addc_u32 s60, s60, 0
	s_cmp_gt_u32 s61, 29
	.p2alignl 6, 3212836864

.LBB0_2365:
	s_ashr_i32 s23, s22, 31
	s_lshl_b64 s[26:27], s[22:23], 19
	s_add_u32 s26, s19, s26
	s_addc_u32 s27, s40, s27
	s_and_b64 s[28:29], s[4:5], exec
	s_cselect_b32 s23, s27, s35
	s_cselect_b32 s66, s26, s34
	s_ashr_i32 s25, s24, 31
	s_lshl_b64 s[28:29], s[24:25], 19
	s_add_u32 s28, s41, s28
	s_addc_u32 s29, s42, s29
	s_and_b64 s[38:39], s[4:5], exec
	s_cselect_b32 s25, s29, s37
	s_cselect_b32 s67, s28, s36
	s_add_u32 s34, s34, 0x40080
	s_addc_u32 s35, s35, 0
	s_add_u32 s68, s36, 0x100
	s_addc_u32 s69, s37, 0
	s_mov_b32 s70, -2
	ds_read_b128 v[18:21], v186
	ds_read_b128 v[22:25], v186 offset:1024
	ds_read_b128 v[26:29], v186 offset:2048
	ds_read_b128 v[30:33], v186 offset:3072
	ds_read_b128 v[2:5], v187
	ds_read_b128 v[6:9], v187 offset:1024
	ds_read_b128 v[10:13], v187 offset:2048
	ds_read_b128 v[14:17], v187 offset:3072
	s_add_u32 s36, s34, 0xfffc0080
	s_addc_u32 s37, s35, -1
	s_cmp_eq_u32 s70, 12
	s_cselect_b32 s39, s23, s37
	s_cselect_b32 s38, s66, s36
	s_cselect_b32 s37, s25, s69
	s_cselect_b32 s36, s67, s68
	v_lshl_add_u64 v[208:209], s[34:35], 0, v[170:171]
	s_add_i32 m0, s31, 0xc000
	ds_read_b128 v[176:179], v188
	ds_read_b128 v[180:183], v188 offset:1024
	ds_read_b128 v[192:195], v188 offset:2048
	ds_read_b128 v[196:199], v188 offset:3072
	ds_read_b128 v[200:203], v188 offset:4096
	ds_read_b128 v[204:207], v188 offset:5120
	ds_read_b128 v[216:219], v188 offset:6144
	ds_read_b128 v[220:223], v188 offset:7168
	global_load_lds_dwordx4 v[208:209], off
	v_lshl_add_u64 v[208:209], s[34:35], 0, v[172:173]
	s_add_i32 m0, s31, 0xe000
	s_nop 0
	global_load_lds_dwordx4 v[208:209], off
	s_waitcnt vmcnt(8)
	s_waitcnt lgkmcnt(0)
	s_setprio 1
	s_barrier
	v_mfma_scale_f32_16x16x128_f8f6f4 v[158:161], v[18:25], v[176:183], 0, v189, v190 op_sel_hi:[0,0,0]
	v_mfma_scale_f32_16x16x128_f8f6f4 v[150:153], v[26:33], v[176:183], 0, v189, v190 op_sel_hi:[0,0,0]
	v_mfma_scale_f32_16x16x128_f8f6f4 v[142:145], v[18:25], v[192:199], 0, v189, v190 op_sel_hi:[0,0,0]
	v_mfma_scale_f32_16x16x128_f8f6f4 v[134:137], v[26:33], v[192:199], 0, v189, v190 op_sel_hi:[0,0,0]
	v_mfma_scale_f32_16x16x128_f8f6f4 v[126:129], v[18:25], v[200:207], 0, v189, v190 op_sel_hi:[0,0,0]
	v_mfma_scale_f32_16x16x128_f8f6f4 v[118:121], v[26:33], v[200:207], 0, v189, v190 op_sel_hi:[0,0,0]
	v_mfma_scale_f32_16x16x128_f8f6f4 v[110:113], v[18:25], v[216:223], 0, v189, v190 op_sel_hi:[0,0,0]
	v_mfma_scale_f32_16x16x128_f8f6f4 v[102:105], v[26:33], v[216:223], 0, v189, v190 op_sel_hi:[0,0,0]
	s_setprio 0
	s_setprio 1
	v_mfma_scale_f32_16x16x128_f8f6f4 v[154:157], v[2:9], v[176:183], 0, v189, v190 op_sel_hi:[0,0,0]
	v_mfma_scale_f32_16x16x128_f8f6f4 v[146:149], v[10:17], v[176:183], 0, v189, v190 op_sel_hi:[0,0,0]
	v_mfma_scale_f32_16x16x128_f8f6f4 v[138:141], v[2:9], v[192:199], 0, v189, v190 op_sel_hi:[0,0,0]
	v_mfma_scale_f32_16x16x128_f8f6f4 v[130:133], v[10:17], v[192:199], 0, v189, v190 op_sel_hi:[0,0,0]
	v_mfma_scale_f32_16x16x128_f8f6f4 v[122:125], v[2:9], v[200:207], 0, v189, v190 op_sel_hi:[0,0,0]
	v_mfma_scale_f32_16x16x128_f8f6f4 v[114:117], v[10:17], v[200:207], 0, v189, v190 op_sel_hi:[0,0,0]
	v_mfma_scale_f32_16x16x128_f8f6f4 v[106:109], v[2:9], v[216:223], 0, v189, v190 op_sel_hi:[0,0,0]
	v_mfma_scale_f32_16x16x128_f8f6f4 v[98:101], v[10:17], v[216:223], 0, v189, v190 op_sel_hi:[0,0,0]
	s_barrier
	s_setprio 0
	s_add_i32 s71, s60, s43
	v_lshl_add_u64 v[176:177], s[36:37], 0, v[166:167]
	s_mov_b32 m0, s71
	ds_read_b128 v[192:195], v188 offset:16384
	ds_read_b128 v[196:199], v188 offset:17408
	ds_read_b128 v[200:203], v188 offset:18432
	ds_read_b128 v[204:207], v188 offset:19456
	ds_read_b128 v[216:219], v188 offset:20480
	ds_read_b128 v[220:223], v188 offset:21504
	ds_read_b128 v[224:227], v188 offset:22528
	ds_read_b128 v[228:231], v188 offset:23552
	global_load_lds_dwordx4 v[176:177], off
	s_add_i32 m0, s71, 0x2000
	s_add_u32 s72, s36, 0x40000
	v_lshl_add_u64 v[178:179], s[36:37], 0, v[162:163]
	s_addc_u32 s73, s37, 0
	s_add_i32 s71, s61, s43
	global_load_lds_dwordx4 v[178:179], off
	v_lshl_add_u64 v[180:181], s[72:73], 0, v[166:167]
	s_mov_b32 m0, s71
	v_lshl_add_u64 v[182:183], s[38:39], 0, v[164:165]
	global_load_lds_dwordx4 v[180:181], off
	v_lshl_add_u64 v[180:181], s[72:73], 0, v[162:163]
	s_add_i32 m0, s71, 0x2000
	s_nop 0
	global_load_lds_dwordx4 v[180:181], off
	v_lshl_add_u64 v[180:181], s[38:39], 0, v[168:169]
	s_mov_b32 m0, s31
	s_nop 0
	global_load_lds_dwordx4 v[180:181], off
	s_mov_b32 m0, s47
	s_nop 0
	global_load_lds_dwordx4 v[182:183], off
	s_waitcnt vmcnt(8)
	s_waitcnt lgkmcnt(0)
	s_setprio 1
	s_barrier
	v_mfma_scale_f32_16x16x128_f8f6f4 v[94:97], v[18:25], v[192:199], 0, v189, v190 op_sel_hi:[0,0,0]
	v_mfma_scale_f32_16x16x128_f8f6f4 v[86:89], v[26:33], v[192:199], 0, v189, v190 op_sel_hi:[0,0,0]
	v_mfma_scale_f32_16x16x128_f8f6f4 v[78:81], v[18:25], v[200:207], 0, v189, v190 op_sel_hi:[0,0,0]
	v_mfma_scale_f32_16x16x128_f8f6f4 v[70:73], v[26:33], v[200:207], 0, v189, v190 op_sel_hi:[0,0,0]
	v_mfma_scale_f32_16x16x128_f8f6f4 v[62:65], v[18:25], v[216:223], 0, v189, v190 op_sel_hi:[0,0,0]
	v_mfma_scale_f32_16x16x128_f8f6f4 v[54:57], v[26:33], v[216:223], 0, v189, v190 op_sel_hi:[0,0,0]
	v_mfma_scale_f32_16x16x128_f8f6f4 v[46:49], v[18:25], v[224:231], 0, v189, v190 op_sel_hi:[0,0,0]
	v_mfma_scale_f32_16x16x128_f8f6f4 v[38:41], v[26:33], v[224:231], 0, v189, v190 op_sel_hi:[0,0,0]
	s_setprio 0
	s_setprio 1
	v_mfma_scale_f32_16x16x128_f8f6f4 v[90:93], v[2:9], v[192:199], 0, v189, v190 op_sel_hi:[0,0,0]
	v_mfma_scale_f32_16x16x128_f8f6f4 v[82:85], v[10:17], v[192:199], 0, v189, v190 op_sel_hi:[0,0,0]
	v_mfma_scale_f32_16x16x128_f8f6f4 v[74:77], v[2:9], v[200:207], 0, v189, v190 op_sel_hi:[0,0,0]
	v_mfma_scale_f32_16x16x128_f8f6f4 v[66:69], v[10:17], v[200:207], 0, v189, v190 op_sel_hi:[0,0,0]
	v_mfma_scale_f32_16x16x128_f8f6f4 v[58:61], v[2:9], v[216:223], 0, v189, v190 op_sel_hi:[0,0,0]
	v_mfma_scale_f32_16x16x128_f8f6f4 v[50:53], v[10:17], v[216:223], 0, v189, v190 op_sel_hi:[0,0,0]
	v_mfma_scale_f32_16x16x128_f8f6f4 v[42:45], v[2:9], v[224:231], 0, v189, v190 op_sel_hi:[0,0,0]
	v_mfma_scale_f32_16x16x128_f8f6f4 v[34:37], v[10:17], v[224:231], 0, v189, v190 op_sel_hi:[0,0,0]
	s_barrier
	s_setprio 0
	s_add_i32 s71, 0, 0x18000
	s_add_i32 s72, 0, 0x1c000
	v_add_u32_e32 v14, s71, v184
	v_add_u32_e32 v30, s72, v184
	ds_read_b128 v[2:5], v14
	ds_read_b128 v[6:9], v14 offset:1024
	ds_read_b128 v[10:13], v14 offset:2048
	ds_read_b128 v[14:17], v14 offset:3072
	ds_read_b128 v[18:21], v30
	ds_read_b128 v[22:25], v30 offset:1024
	ds_read_b128 v[26:29], v30 offset:2048
	ds_read_b128 v[30:33], v30 offset:3072
	s_add_u32 s38, s38, 0x40000
	s_addc_u32 s39, s39, 0
	s_mov_b32 m0, s48
	v_lshl_add_u64 v[208:209], s[38:39], 0, v[168:169]
	ds_read_b128 v[192:195], v188 offset:32768
	ds_read_b128 v[196:199], v188 offset:33792
	ds_read_b128 v[200:203], v188 offset:34816
	ds_read_b128 v[204:207], v188 offset:35840
	ds_read_b128 v[216:219], v188 offset:36864
	ds_read_b128 v[220:223], v188 offset:37888
	ds_read_b128 v[224:227], v188 offset:38912
	ds_read_b128 v[228:231], v188 offset:39936
	global_load_lds_dwordx4 v[208:209], off
	v_lshl_add_u64 v[208:209], s[38:39], 0, v[164:165]
	s_mov_b32 m0, s49
	s_nop 0
	global_load_lds_dwordx4 v[208:209], off
	s_waitcnt vmcnt(8)
	s_waitcnt lgkmcnt(0)
	s_setprio 1
	s_barrier
	v_mfma_scale_f32_16x16x128_f8f6f4 v[158:161], v[2:9], v[192:199], v[158:161], v189, v190 op_sel_hi:[0,0,0]
	v_mfma_scale_f32_16x16x128_f8f6f4 v[150:153], v[10:17], v[192:199], v[150:153], v189, v190 op_sel_hi:[0,0,0]
	v_mfma_scale_f32_16x16x128_f8f6f4 v[142:145], v[2:9], v[200:207], v[142:145], v189, v190 op_sel_hi:[0,0,0]
	v_mfma_scale_f32_16x16x128_f8f6f4 v[134:137], v[10:17], v[200:207], v[134:137], v189, v190 op_sel_hi:[0,0,0]
	v_mfma_scale_f32_16x16x128_f8f6f4 v[126:129], v[2:9], v[216:223], v[126:129], v189, v190 op_sel_hi:[0,0,0]
	v_mfma_scale_f32_16x16x128_f8f6f4 v[118:121], v[10:17], v[216:223], v[118:121], v189, v190 op_sel_hi:[0,0,0]
	v_mfma_scale_f32_16x16x128_f8f6f4 v[110:113], v[2:9], v[224:231], v[110:113], v189, v190 op_sel_hi:[0,0,0]
	v_mfma_scale_f32_16x16x128_f8f6f4 v[102:105], v[10:17], v[224:231], v[102:105], v189, v190 op_sel_hi:[0,0,0]
	s_setprio 0
	s_setprio 1
	v_mfma_scale_f32_16x16x128_f8f6f4 v[154:157], v[18:25], v[192:199], v[154:157], v189, v190 op_sel_hi:[0,0,0]
	v_mfma_scale_f32_16x16x128_f8f6f4 v[146:149], v[26:33], v[192:199], v[146:149], v189, v190 op_sel_hi:[0,0,0]
	v_mfma_scale_f32_16x16x128_f8f6f4 v[138:141], v[18:25], v[200:207], v[138:141], v189, v190 op_sel_hi:[0,0,0]
	v_mfma_scale_f32_16x16x128_f8f6f4 v[130:133], v[26:33], v[200:207], v[130:133], v189, v190 op_sel_hi:[0,0,0]
	v_mfma_scale_f32_16x16x128_f8f6f4 v[122:125], v[18:25], v[216:223], v[122:125], v189, v190 op_sel_hi:[0,0,0]
	v_mfma_scale_f32_16x16x128_f8f6f4 v[114:117], v[26:33], v[216:223], v[114:117], v189, v190 op_sel_hi:[0,0,0]
	v_mfma_scale_f32_16x16x128_f8f6f4 v[106:109], v[18:25], v[224:231], v[106:109], v189, v190 op_sel_hi:[0,0,0]
	v_mfma_scale_f32_16x16x128_f8f6f4 v[98:101], v[26:33], v[224:231], v[98:101], v189, v190 op_sel_hi:[0,0,0]
	s_barrier
	s_setprio 0
	s_add_i32 s38, s71, s43
	v_lshl_add_u64 v[176:177], v[176:177], 0, s[12:13]
	s_mov_b32 m0, s38
	ds_read_b128 v[192:195], v188 offset:49152
	ds_read_b128 v[196:199], v188 offset:50176
	ds_read_b128 v[200:203], v188 offset:51200
	ds_read_b128 v[204:207], v188 offset:52224
	ds_read_b128 v[216:219], v188 offset:53248
	ds_read_b128 v[220:223], v188 offset:54272
	ds_read_b128 v[224:227], v188 offset:55296
	ds_read_b128 v[228:231], v188 offset:56320
	global_load_lds_dwordx4 v[176:177], off
	s_add_i32 m0, s38, 0x2000
	s_add_u32 s36, s36, 0x40080
	v_lshl_add_u64 v[176:177], v[178:179], 0, s[12:13]
	s_addc_u32 s37, s37, 0
	s_add_i32 s38, s72, s43
	global_load_lds_dwordx4 v[176:177], off
	v_lshl_add_u64 v[176:177], s[36:37], 0, v[166:167]
	s_mov_b32 m0, s38
	s_nop 0
	global_load_lds_dwordx4 v[176:177], off
	v_lshl_add_u64 v[176:177], s[36:37], 0, v[162:163]
	s_add_i32 m0, s38, 0x2000
	s_nop 0
	global_load_lds_dwordx4 v[176:177], off
	v_lshl_add_u64 v[176:177], v[180:181], 0, s[12:13]
	s_mov_b32 m0, s50
	s_nop 0
	global_load_lds_dwordx4 v[176:177], off
	v_lshl_add_u64 v[176:177], v[182:183], 0, s[12:13]
	s_mov_b32 m0, s51
	s_nop 0
	global_load_lds_dwordx4 v[176:177], off
	s_waitcnt vmcnt(8)
	s_waitcnt lgkmcnt(0)
	s_setprio 1
	s_barrier
	v_mfma_scale_f32_16x16x128_f8f6f4 v[94:97], v[2:9], v[192:199], v[94:97], v189, v190 op_sel_hi:[0,0,0]
	v_mfma_scale_f32_16x16x128_f8f6f4 v[86:89], v[10:17], v[192:199], v[86:89], v189, v190 op_sel_hi:[0,0,0]
	v_mfma_scale_f32_16x16x128_f8f6f4 v[78:81], v[2:9], v[200:207], v[78:81], v189, v190 op_sel_hi:[0,0,0]
	v_mfma_scale_f32_16x16x128_f8f6f4 v[70:73], v[10:17], v[200:207], v[70:73], v189, v190 op_sel_hi:[0,0,0]
	v_mfma_scale_f32_16x16x128_f8f6f4 v[62:65], v[2:9], v[216:223], v[62:65], v189, v190 op_sel_hi:[0,0,0]
	v_mfma_scale_f32_16x16x128_f8f6f4 v[54:57], v[10:17], v[216:223], v[54:57], v189, v190 op_sel_hi:[0,0,0]
	v_mfma_scale_f32_16x16x128_f8f6f4 v[46:49], v[2:9], v[224:231], v[46:49], v189, v190 op_sel_hi:[0,0,0]
	v_mfma_scale_f32_16x16x128_f8f6f4 v[38:41], v[10:17], v[224:231], v[38:41], v189, v190 op_sel_hi:[0,0,0]
	s_setprio 0
	s_setprio 1
	v_mfma_scale_f32_16x16x128_f8f6f4 v[90:93], v[18:25], v[192:199], v[90:93], v189, v190 op_sel_hi:[0,0,0]
	v_mfma_scale_f32_16x16x128_f8f6f4 v[82:85], v[26:33], v[192:199], v[82:85], v189, v190 op_sel_hi:[0,0,0]
	v_mfma_scale_f32_16x16x128_f8f6f4 v[74:77], v[18:25], v[200:207], v[74:77], v189, v190 op_sel_hi:[0,0,0]
	v_mfma_scale_f32_16x16x128_f8f6f4 v[66:69], v[26:33], v[200:207], v[66:69], v189, v190 op_sel_hi:[0,0,0]
	v_mfma_scale_f32_16x16x128_f8f6f4 v[58:61], v[18:25], v[216:223], v[58:61], v189, v190 op_sel_hi:[0,0,0]
	v_mfma_scale_f32_16x16x128_f8f6f4 v[50:53], v[26:33], v[216:223], v[50:53], v189, v190 op_sel_hi:[0,0,0]
	v_mfma_scale_f32_16x16x128_f8f6f4 v[42:45], v[18:25], v[224:231], v[42:45], v189, v190 op_sel_hi:[0,0,0]
	v_mfma_scale_f32_16x16x128_f8f6f4 v[34:37], v[26:33], v[224:231], v[34:37], v189, v190 op_sel_hi:[0,0,0]
	s_barrier
	s_setprio 0
	s_add_i32 s70, s70, 2
	s_add_u32 s34, s34, 0x100
	s_addc_u32 s35, s35, 0
	s_add_u32 s68, s68, 0x100
	s_addc_u32 s69, s69, 0
	s_cmp_gt_u32 s70, 13
	.p2alignl 6, 3212836864

.LBB0_2440:
	s_add_u32 s38, s38, 0xe0080
	s_addc_u32 s39, s39, 0
	v_lshl_add_u64 v[176:177], v[0:1], 0, s[26:27]
	s_mov_b32 s71, -2
	ds_read_b128 v[16:19], v191
	ds_read_b128 v[20:23], v191 offset:1024
	ds_read_b128 v[24:27], v191 offset:2048
	ds_read_b128 v[28:31], v191 offset:3072
	ds_read_b128 v[0:3], v192
	ds_read_b128 v[4:7], v192 offset:1024
	ds_read_b128 v[8:11], v192 offset:2048
	ds_read_b128 v[12:15], v192 offset:3072
	s_add_u32 s40, s38, 0xfff20080
	s_addc_u32 s41, s39, -1
	s_cmp_eq_u32 s71, 52
	s_cselect_b64 vcc, -1, 0
	s_cselect_b32 s41, s1, s41
	s_cselect_b32 s40, s0, s40
	v_cndmask_b32_e32 v179, v177, v175, vcc
	v_cndmask_b32_e32 v178, v176, v174, vcc
	v_lshl_add_u64 v[214:215], s[38:39], 0, v[168:169]
	s_add_i32 m0, s47, 0xc000
	ds_read_b128 v[180:183], v193
	ds_read_b128 v[184:187], v193 offset:1024
	ds_read_b128 v[198:201], v193 offset:2048
	ds_read_b128 v[202:205], v193 offset:3072
	ds_read_b128 v[206:209], v193 offset:4096
	ds_read_b128 v[210:213], v193 offset:5120
	ds_read_b128 v[216:219], v193 offset:6144
	ds_read_b128 v[220:223], v193 offset:7168
	global_load_lds_dwordx4 v[214:215], off
	v_lshl_add_u64 v[214:215], s[38:39], 0, v[170:171]
	s_add_i32 m0, s47, 0xe000
	s_nop 0
	global_load_lds_dwordx4 v[214:215], off
	s_waitcnt vmcnt(8)
	s_waitcnt lgkmcnt(0)
	s_setprio 1
	s_barrier
	v_mfma_scale_f32_16x16x128_f8f6f4 v[156:159], v[16:23], v[180:187], 0, v194, v195 op_sel_hi:[0,0,0]
	v_mfma_scale_f32_16x16x128_f8f6f4 v[152:155], v[24:31], v[180:187], 0, v194, v195 op_sel_hi:[0,0,0]
	v_mfma_scale_f32_16x16x128_f8f6f4 v[148:151], v[16:23], v[198:205], 0, v194, v195 op_sel_hi:[0,0,0]
	v_mfma_scale_f32_16x16x128_f8f6f4 v[140:143], v[24:31], v[198:205], 0, v194, v195 op_sel_hi:[0,0,0]
	v_mfma_scale_f32_16x16x128_f8f6f4 v[132:135], v[16:23], v[206:213], 0, v194, v195 op_sel_hi:[0,0,0]
	v_mfma_scale_f32_16x16x128_f8f6f4 v[124:127], v[24:31], v[206:213], 0, v194, v195 op_sel_hi:[0,0,0]
	v_mfma_scale_f32_16x16x128_f8f6f4 v[116:119], v[16:23], v[216:223], 0, v194, v195 op_sel_hi:[0,0,0]
	v_mfma_scale_f32_16x16x128_f8f6f4 v[108:111], v[24:31], v[216:223], 0, v194, v195 op_sel_hi:[0,0,0]
	s_setprio 0
	s_setprio 1
	v_mfma_scale_f32_16x16x128_f8f6f4 v[144:147], v[0:7], v[180:187], 0, v194, v195 op_sel_hi:[0,0,0]
	v_mfma_scale_f32_16x16x128_f8f6f4 v[136:139], v[8:15], v[180:187], 0, v194, v195 op_sel_hi:[0,0,0]
	v_mfma_scale_f32_16x16x128_f8f6f4 v[128:131], v[0:7], v[198:205], 0, v194, v195 op_sel_hi:[0,0,0]
	v_mfma_scale_f32_16x16x128_f8f6f4 v[120:123], v[8:15], v[198:205], 0, v194, v195 op_sel_hi:[0,0,0]
	v_mfma_scale_f32_16x16x128_f8f6f4 v[112:115], v[0:7], v[206:213], 0, v194, v195 op_sel_hi:[0,0,0]
	v_mfma_scale_f32_16x16x128_f8f6f4 v[104:107], v[8:15], v[206:213], 0, v194, v195 op_sel_hi:[0,0,0]
	v_mfma_scale_f32_16x16x128_f8f6f4 v[100:103], v[0:7], v[216:223], 0, v194, v195 op_sel_hi:[0,0,0]
	v_mfma_scale_f32_16x16x128_f8f6f4 v[96:99], v[8:15], v[216:223], 0, v194, v195 op_sel_hi:[0,0,0]
	s_barrier
	s_setprio 0
	s_add_i32 s72, s6, s44
	v_lshl_add_u64 v[180:181], v[178:179], 0, v[164:165]
	s_mov_b32 m0, s72
	ds_read_b128 v[198:201], v193 offset:16384
	ds_read_b128 v[202:205], v193 offset:17408
	ds_read_b128 v[206:209], v193 offset:18432
	ds_read_b128 v[210:213], v193 offset:19456
	ds_read_b128 v[216:219], v193 offset:20480
	ds_read_b128 v[220:223], v193 offset:21504
	ds_read_b128 v[224:227], v193 offset:22528
	ds_read_b128 v[228:231], v193 offset:23552
	global_load_lds_dwordx4 v[180:181], off
	v_lshl_add_u64 v[182:183], v[178:179], 0, v[160:161]
	s_add_i32 m0, s72, 0x2000
	v_lshl_add_u64 v[184:185], v[178:179], 0, s[10:11]
	s_add_i32 s72, s62, s44
	global_load_lds_dwordx4 v[182:183], off
	v_lshl_add_u64 v[186:187], v[184:185], 0, v[164:165]
	s_mov_b32 m0, s72
	v_lshl_add_u64 v[184:185], v[184:185], 0, v[160:161]
	global_load_lds_dwordx4 v[186:187], off
	s_add_i32 m0, s72, 0x2000
	v_lshl_add_u64 v[186:187], s[40:41], 0, v[162:163]
	global_load_lds_dwordx4 v[184:185], off
	v_lshl_add_u64 v[184:185], s[40:41], 0, v[166:167]
	s_mov_b32 m0, s47
	s_nop 0
	global_load_lds_dwordx4 v[184:185], off
	s_mov_b32 m0, s48
	s_nop 0
	global_load_lds_dwordx4 v[186:187], off
	s_waitcnt vmcnt(8)
	s_waitcnt lgkmcnt(0)
	s_setprio 1
	s_barrier
	v_mfma_scale_f32_16x16x128_f8f6f4 v[92:95], v[16:23], v[198:205], 0, v194, v195 op_sel_hi:[0,0,0]
	v_mfma_scale_f32_16x16x128_f8f6f4 v[88:91], v[24:31], v[198:205], 0, v194, v195 op_sel_hi:[0,0,0]
	v_mfma_scale_f32_16x16x128_f8f6f4 v[84:87], v[16:23], v[206:213], 0, v194, v195 op_sel_hi:[0,0,0]
	v_mfma_scale_f32_16x16x128_f8f6f4 v[76:79], v[24:31], v[206:213], 0, v194, v195 op_sel_hi:[0,0,0]
	v_mfma_scale_f32_16x16x128_f8f6f4 v[68:71], v[16:23], v[216:223], 0, v194, v195 op_sel_hi:[0,0,0]
	v_mfma_scale_f32_16x16x128_f8f6f4 v[60:63], v[24:31], v[216:223], 0, v194, v195 op_sel_hi:[0,0,0]
	v_mfma_scale_f32_16x16x128_f8f6f4 v[52:55], v[16:23], v[224:231], 0, v194, v195 op_sel_hi:[0,0,0]
	v_mfma_scale_f32_16x16x128_f8f6f4 v[44:47], v[24:31], v[224:231], 0, v194, v195 op_sel_hi:[0,0,0]
	s_setprio 0
	s_setprio 1
	v_mfma_scale_f32_16x16x128_f8f6f4 v[80:83], v[0:7], v[198:205], 0, v194, v195 op_sel_hi:[0,0,0]
	v_mfma_scale_f32_16x16x128_f8f6f4 v[72:75], v[8:15], v[198:205], 0, v194, v195 op_sel_hi:[0,0,0]
	v_mfma_scale_f32_16x16x128_f8f6f4 v[64:67], v[0:7], v[206:213], 0, v194, v195 op_sel_hi:[0,0,0]
	v_mfma_scale_f32_16x16x128_f8f6f4 v[56:59], v[8:15], v[206:213], 0, v194, v195 op_sel_hi:[0,0,0]
	v_mfma_scale_f32_16x16x128_f8f6f4 v[48:51], v[0:7], v[216:223], 0, v194, v195 op_sel_hi:[0,0,0]
	v_mfma_scale_f32_16x16x128_f8f6f4 v[40:43], v[8:15], v[216:223], 0, v194, v195 op_sel_hi:[0,0,0]
	v_mfma_scale_f32_16x16x128_f8f6f4 v[36:39], v[0:7], v[224:231], 0, v194, v195 op_sel_hi:[0,0,0]
	v_mfma_scale_f32_16x16x128_f8f6f4 v[32:35], v[8:15], v[224:231], 0, v194, v195 op_sel_hi:[0,0,0]
	s_barrier
	s_setprio 0
	s_add_i32 s72, 0, 0x18000
	s_add_i32 s73, 0, 0x1c000
	v_add_u32_e32 v12, s72, v189
	v_add_u32_e32 v28, s73, v189
	ds_read_b128 v[0:3], v12
	ds_read_b128 v[4:7], v12 offset:1024
	ds_read_b128 v[8:11], v12 offset:2048
	ds_read_b128 v[12:15], v12 offset:3072
	ds_read_b128 v[16:19], v28
	ds_read_b128 v[20:23], v28 offset:1024
	ds_read_b128 v[24:27], v28 offset:2048
	ds_read_b128 v[28:31], v28 offset:3072
	s_add_u32 s40, s40, 0xe0000
	s_addc_u32 s41, s41, 0
	s_mov_b32 m0, s49
	v_lshl_add_u64 v[214:215], s[40:41], 0, v[166:167]
	ds_read_b128 v[198:201], v193 offset:32768
	ds_read_b128 v[202:205], v193 offset:33792
	ds_read_b128 v[206:209], v193 offset:34816
	ds_read_b128 v[210:213], v193 offset:35840
	ds_read_b128 v[216:219], v193 offset:36864
	ds_read_b128 v[220:223], v193 offset:37888
	ds_read_b128 v[224:227], v193 offset:38912
	ds_read_b128 v[228:231], v193 offset:39936
	global_load_lds_dwordx4 v[214:215], off
	v_lshl_add_u64 v[214:215], s[40:41], 0, v[162:163]
	s_mov_b32 m0, s50
	s_nop 0
	global_load_lds_dwordx4 v[214:215], off
	s_waitcnt vmcnt(8)
	s_waitcnt lgkmcnt(0)
	s_setprio 1
	s_barrier
	v_mfma_scale_f32_16x16x128_f8f6f4 v[156:159], v[0:7], v[198:205], v[156:159], v194, v195 op_sel_hi:[0,0,0]
	v_mfma_scale_f32_16x16x128_f8f6f4 v[152:155], v[8:15], v[198:205], v[152:155], v194, v195 op_sel_hi:[0,0,0]
	v_mfma_scale_f32_16x16x128_f8f6f4 v[148:151], v[0:7], v[206:213], v[148:151], v194, v195 op_sel_hi:[0,0,0]
	v_mfma_scale_f32_16x16x128_f8f6f4 v[140:143], v[8:15], v[206:213], v[140:143], v194, v195 op_sel_hi:[0,0,0]
	v_mfma_scale_f32_16x16x128_f8f6f4 v[132:135], v[0:7], v[216:223], v[132:135], v194, v195 op_sel_hi:[0,0,0]
	v_mfma_scale_f32_16x16x128_f8f6f4 v[124:127], v[8:15], v[216:223], v[124:127], v194, v195 op_sel_hi:[0,0,0]
	v_mfma_scale_f32_16x16x128_f8f6f4 v[116:119], v[0:7], v[224:231], v[116:119], v194, v195 op_sel_hi:[0,0,0]
	v_mfma_scale_f32_16x16x128_f8f6f4 v[108:111], v[8:15], v[224:231], v[108:111], v194, v195 op_sel_hi:[0,0,0]
	s_setprio 0
	s_setprio 1
	v_mfma_scale_f32_16x16x128_f8f6f4 v[144:147], v[16:23], v[198:205], v[144:147], v194, v195 op_sel_hi:[0,0,0]
	v_mfma_scale_f32_16x16x128_f8f6f4 v[136:139], v[24:31], v[198:205], v[136:139], v194, v195 op_sel_hi:[0,0,0]
	v_mfma_scale_f32_16x16x128_f8f6f4 v[128:131], v[16:23], v[206:213], v[128:131], v194, v195 op_sel_hi:[0,0,0]
	v_mfma_scale_f32_16x16x128_f8f6f4 v[120:123], v[24:31], v[206:213], v[120:123], v194, v195 op_sel_hi:[0,0,0]
	v_mfma_scale_f32_16x16x128_f8f6f4 v[112:115], v[16:23], v[216:223], v[112:115], v194, v195 op_sel_hi:[0,0,0]
	v_mfma_scale_f32_16x16x128_f8f6f4 v[104:107], v[24:31], v[216:223], v[104:107], v194, v195 op_sel_hi:[0,0,0]
	v_mfma_scale_f32_16x16x128_f8f6f4 v[100:103], v[16:23], v[224:231], v[100:103], v194, v195 op_sel_hi:[0,0,0]
	v_mfma_scale_f32_16x16x128_f8f6f4 v[96:99], v[24:31], v[224:231], v[96:99], v194, v195 op_sel_hi:[0,0,0]
	s_barrier
	s_setprio 0
	s_add_i32 s40, s72, s44
	v_lshl_add_u64 v[180:181], v[180:181], 0, s[18:19]
	s_mov_b32 m0, s40
	ds_read_b128 v[198:201], v193 offset:49152
	ds_read_b128 v[202:205], v193 offset:50176
	ds_read_b128 v[206:209], v193 offset:51200
	ds_read_b128 v[210:213], v193 offset:52224
	ds_read_b128 v[216:219], v193 offset:53248
	ds_read_b128 v[220:223], v193 offset:54272
	ds_read_b128 v[224:227], v193 offset:55296
	ds_read_b128 v[228:231], v193 offset:56320
	global_load_lds_dwordx4 v[180:181], off
	v_lshl_add_u64 v[180:181], v[182:183], 0, s[18:19]
	s_add_i32 m0, s40, 0x2000
	v_lshl_add_u64 v[178:179], v[178:179], 0, s[22:23]
	s_add_i32 s40, s73, s44
	global_load_lds_dwordx4 v[180:181], off
	v_lshl_add_u64 v[180:181], v[178:179], 0, v[164:165]
	s_mov_b32 m0, s40
	v_lshl_add_u64 v[178:179], v[178:179], 0, v[160:161]
	global_load_lds_dwordx4 v[180:181], off
	s_add_i32 m0, s40, 0x2000
	s_nop 0
	global_load_lds_dwordx4 v[178:179], off
	v_lshl_add_u64 v[178:179], v[184:185], 0, s[18:19]
	s_mov_b32 m0, s59
	s_nop 0
	global_load_lds_dwordx4 v[178:179], off
	v_lshl_add_u64 v[178:179], v[186:187], 0, s[18:19]
	s_mov_b32 m0, s60
	s_nop 0
	global_load_lds_dwordx4 v[178:179], off
	s_waitcnt vmcnt(8)
	s_waitcnt lgkmcnt(0)
	s_setprio 1
	s_barrier
	v_mfma_scale_f32_16x16x128_f8f6f4 v[92:95], v[0:7], v[198:205], v[92:95], v194, v195 op_sel_hi:[0,0,0]
	v_mfma_scale_f32_16x16x128_f8f6f4 v[88:91], v[8:15], v[198:205], v[88:91], v194, v195 op_sel_hi:[0,0,0]
	v_mfma_scale_f32_16x16x128_f8f6f4 v[84:87], v[0:7], v[206:213], v[84:87], v194, v195 op_sel_hi:[0,0,0]
	v_mfma_scale_f32_16x16x128_f8f6f4 v[76:79], v[8:15], v[206:213], v[76:79], v194, v195 op_sel_hi:[0,0,0]
	v_mfma_scale_f32_16x16x128_f8f6f4 v[68:71], v[0:7], v[216:223], v[68:71], v194, v195 op_sel_hi:[0,0,0]
	v_mfma_scale_f32_16x16x128_f8f6f4 v[60:63], v[8:15], v[216:223], v[60:63], v194, v195 op_sel_hi:[0,0,0]
	v_mfma_scale_f32_16x16x128_f8f6f4 v[52:55], v[0:7], v[224:231], v[52:55], v194, v195 op_sel_hi:[0,0,0]
	v_mfma_scale_f32_16x16x128_f8f6f4 v[44:47], v[8:15], v[224:231], v[44:47], v194, v195 op_sel_hi:[0,0,0]
	s_setprio 0
	s_setprio 1
	v_mfma_scale_f32_16x16x128_f8f6f4 v[80:83], v[16:23], v[198:205], v[80:83], v194, v195 op_sel_hi:[0,0,0]
	v_mfma_scale_f32_16x16x128_f8f6f4 v[72:75], v[24:31], v[198:205], v[72:75], v194, v195 op_sel_hi:[0,0,0]
	v_mfma_scale_f32_16x16x128_f8f6f4 v[64:67], v[16:23], v[206:213], v[64:67], v194, v195 op_sel_hi:[0,0,0]
	v_mfma_scale_f32_16x16x128_f8f6f4 v[56:59], v[24:31], v[206:213], v[56:59], v194, v195 op_sel_hi:[0,0,0]
	v_mfma_scale_f32_16x16x128_f8f6f4 v[48:51], v[16:23], v[216:223], v[48:51], v194, v195 op_sel_hi:[0,0,0]
	v_mfma_scale_f32_16x16x128_f8f6f4 v[40:43], v[24:31], v[216:223], v[40:43], v194, v195 op_sel_hi:[0,0,0]
	v_mfma_scale_f32_16x16x128_f8f6f4 v[36:39], v[16:23], v[224:231], v[36:39], v194, v195 op_sel_hi:[0,0,0]
	v_mfma_scale_f32_16x16x128_f8f6f4 v[32:35], v[24:31], v[224:231], v[32:35], v194, v195 op_sel_hi:[0,0,0]
	s_barrier
	s_setprio 0
	s_add_i32 s71, s71, 2
	s_add_u32 s38, s38, 0x100
	s_addc_u32 s39, s39, 0
	s_cmp_gt_u32 s71, 53
	v_lshl_add_u64 v[176:177], v[176:177], 0, s[26:27]
	.p2alignl 6, 3212836864
